# merge gates stored fragment-major (each wave store/load instruction covers 512 contiguous bytes instead of 16 rows x 32 B); P3 hook halves aligned
# speedup vs baseline: 1.0232x; 1.0232x over previous
;     template <int ACT, int AUX> __device__ __forceinline__ void run(const f32x4 (&acc)[2][2][4][2], const Unit& uu, int wr, int wc, int fr, int fq) const {
;     ...
;         const int row0 = u.pm * BM + wr * 64 + fr, col0 = u.pn * BM + wc * 32 + 8 * fq;
;         float rsv[8];
; #pragma unroll
;         for (int i = 0; i < 8; ++i) rsv[i] = ss[row0 + (i >> 2) * HALF + (i & 3) * 16];
;         asm volatile("" ::: "memory");
; #pragma unroll
;         for (int i = 0; i < 8; ++i) rsv[i] = __builtin_amdgcn_rsqf(rsv[i] * (1.0f / cfg::DM) + cfg::RMS_EPS);
;         float cs[2][8]; float mx[2][2];
;         if (AUX == 1) {
; #pragma unroll
;             for (int i = 0; i < 16; ++i) cs[i >> 3][i & 7] = 0.f; }
;         if (AUX == 2) { mx[0][0] = mx[0][1] = mx[1][0] = mx[1][1] = 0.f; }
; #pragma unroll
;         for (int ai = 0; ai < 2; ++ai)
; #pragma unroll
;             for (int m = 0; m < 4; ++m) { const int r = row0 + ai * HALF + m * 16; const float rs = rsv[ai * 4 + m];
;                 bf16_t* rowp = O + (size_t)r * cfg::NC + col0; float s1 = 0.f, s2 = 0.f;
; #pragma unroll
;                 for (int bj = 0; bj < 2; ++bj) { f32x4 v0 = acc[ai][bj][m][0] * rs, v1 = acc[ai][bj][m][1] * rs;
; #pragma unroll
;                     for (int j = 0; j < 4; ++j) { v0[j] = act_f<ACT>(v0[j]); v1[j] = act_f<ACT>(v1[j]); }
;                     if (AUX == 4) {
;                         unsigned q[8];
; #pragma unroll
;                         for (int j = 0; j < 4; ++j) { q[j] = (unsigned)fminf(fmaxf(fmaf(v0[j], 255.0f, 0.5f), 1.0f), 255.0f); q[4 + j] = (unsigned)fminf(fmaxf(fmaf(v1[j], 255.0f, 0.5f), 1.0f), 255.0f); }
;                         u32x2 w8; w8.x = q[0] | (q[1] << 8) | (q[2] << 16) | (q[3] << 24); w8.y = q[4] | (q[5] << 8) | (q[6] << 16) | (q[7] << 24);
;                         __builtin_nontemporal_store(w8, (u32x2*)(g8 + ((size_t)((u.pn - 52) >> 4) * cfg::MT + r) * cfg::DM + ((u.pn - 52) & 15) * BM + wc * 32 + 8 * fq + bj * HALF));
.LBB0_157:
	v_lshl_add_u32 v156, s2, 8, v1
	v_ashrrev_i32_e32 v157, 31, v156
	s_waitcnt lgkmcnt(0)
	v_lshl_add_u64 v[146:147], v[156:157], 2, s[22:23]
	global_load_dword v150, v[146:147], off
	global_load_dword v151, v[146:147], off offset:64
	global_load_dword v152, v[146:147], off offset:128
	global_load_dword v153, v[146:147], off offset:192
	global_load_dword v154, v[146:147], off offset:512
	global_load_dword v155, v[146:147], off offset:576
	global_load_dword v158, v[146:147], off offset:640
	global_load_dword v159, v[146:147], off offset:704
	s_lshl_b32 s100, s2, 20
	s_sub_i32 s12, s1, 52
	s_lshr_b32 s2, s12, 4
	s_lshl_b32 s39, s12, 8
	s_lshl_b64 s[12:13], s[2:3], 25
	s_and_b32 s2, s39, 0xf00
	s_add_u32 s12, s63, s12
	s_addc_u32 s13, s64, s13
	s_lshl_b32 s101, s2, 8
	s_add_i32 s100, s100, s101
	s_lshl_b32 s101, s58, 3
	s_add_i32 s100, s100, s101
	s_addk_i32 s100, 0x1000
	s_add_u32 s100, s12, s100
	s_addc_u32 s101, s13, 0
	v_mbcnt_lo_u32_b32 v148, -1, 0
	v_mbcnt_hi_u32_b32 v148, -1, v148
	v_lshlrev_b32_e32 v148, 3, v148
	v_mov_b32_e32 v149, 0
	v_lshl_add_u64 v[148:149], s[100:101], 0, v[148:149]
	s_mov_b32 s39, 0x437f0000
	s_waitcnt vmcnt(0)
	v_fmamk_f32 v146, v150, 0x39800000, v221
	v_rsq_f32_e32 v164, v146
	v_fmamk_f32 v147, v151, 0x39800000, v221
	v_rsq_f32_e32 v162, v147
	v_fmamk_f32 v150, v152, 0x39800000, v221
	v_pk_mul_f32 v[128:129], v[128:129], v[164:165] op_sel_hi:[1,0]
	v_pk_mul_f32 v[124:125], v[124:125], v[164:165] op_sel_hi:[1,0]
	v_pk_mul_f32 v[130:131], v[130:131], v[164:165] op_sel_hi:[1,0]
	v_pk_mul_f32 v[126:127], v[126:127], v[164:165] op_sel_hi:[1,0]
	v_mul_f32_e32 v128, 0xbfb8aa3b, v128
	v_mul_f32_e32 v124, 0xbfb8aa3b, v124
	v_mul_f32_e32 v129, 0xbfb8aa3b, v129
	v_mul_f32_e32 v125, 0xbfb8aa3b, v125
	v_mul_f32_e32 v130, 0xbfb8aa3b, v130
	v_mul_f32_e32 v126, 0xbfb8aa3b, v126
	v_mul_f32_e32 v131, 0xbfb8aa3b, v131
	v_mul_f32_e32 v127, 0xbfb8aa3b, v127
	v_exp_f32_e32 v128, v128
	v_exp_f32_e32 v124, v124
	v_exp_f32_e32 v129, v129
	v_exp_f32_e32 v125, v125
	v_exp_f32_e32 v130, v130
	v_exp_f32_e32 v126, v126
	v_exp_f32_e32 v131, v131
	v_exp_f32_e32 v127, v127
	v_pk_mul_f32 v[116:117], v[116:117], v[164:165] op_sel_hi:[1,0]
	v_add_f32_e32 v128, 1.0, v128
	v_add_f32_e32 v124, 1.0, v124
	v_add_f32_e32 v129, 1.0, v129
	v_add_f32_e32 v125, 1.0, v125
	v_add_f32_e32 v130, 1.0, v130
	v_add_f32_e32 v126, 1.0, v126
	v_add_f32_e32 v131, 1.0, v131
	v_add_f32_e32 v127, 1.0, v127
	v_rcp_f32_e32 v128, v128
	v_rcp_f32_e32 v124, v124
	v_rcp_f32_e32 v129, v129
	v_rcp_f32_e32 v125, v125
	v_mul_f32_e32 v116, 0xbfb8aa3b, v116
	v_pk_mul_f32 v[120:121], v[120:121], v[164:165] op_sel_hi:[1,0]
	v_rcp_f32_e32 v130, v130
	v_rcp_f32_e32 v126, v126
	v_rcp_f32_e32 v131, v131
	v_rcp_f32_e32 v127, v127
	v_exp_f32_e32 v116, v116
	v_pk_mul_f32 v[118:119], v[118:119], v[164:165] op_sel_hi:[1,0]
	v_mul_f32_e32 v117, 0xbfb8aa3b, v117
	v_pk_mul_f32 v[122:123], v[122:123], v[164:165] op_sel_hi:[1,0]
	v_mul_f32_e32 v120, 0xbfb8aa3b, v120
	v_mul_f32_e32 v121, 0xbfb8aa3b, v121
	v_exp_f32_e32 v117, v117
	v_mul_f32_e32 v118, 0xbfb8aa3b, v118
	v_mul_f32_e32 v119, 0xbfb8aa3b, v119
	v_exp_f32_e32 v120, v120
	v_exp_f32_e32 v121, v121
	v_mul_f32_e32 v122, 0xbfb8aa3b, v122
	v_exp_f32_e32 v118, v118
	v_mul_f32_e32 v123, 0xbfb8aa3b, v123
	v_exp_f32_e32 v119, v119
	v_fma_f32 v128, v128, s39, 0.5
	v_fma_f32 v124, v124, s39, 0.5
	v_fma_f32 v129, v129, s39, 0.5
	v_fma_f32 v125, v125, s39, 0.5
	v_exp_f32_e32 v122, v122
	v_exp_f32_e32 v123, v123
	v_fma_f32 v130, v130, s39, 0.5
	v_fma_f32 v126, v126, s39, 0.5
	v_fma_f32 v131, v131, s39, 0.5
	v_fma_f32 v127, v127, s39, 0.5
	v_med3_f32 v128, v128, 1.0, v231
	v_med3_f32 v124, v124, 1.0, v231
	v_med3_f32 v129, v129, 1.0, v231
	v_med3_f32 v125, v125, 1.0, v231
	v_add_f32_e32 v116, 1.0, v116
	v_pk_mul_f32 v[108:109], v[108:109], v[162:163] op_sel_hi:[1,0]
	v_med3_f32 v130, v130, 1.0, v231
	v_med3_f32 v126, v126, 1.0, v231
	v_med3_f32 v131, v131, 1.0, v231
	v_med3_f32 v127, v127, 1.0, v231
	v_cvt_u32_f32_e32 v128, v128
	v_cvt_u32_f32_e32 v124, v124
	v_cvt_u32_f32_e32 v129, v129
	v_cvt_u32_f32_e32 v125, v125
	v_rcp_f32_e32 v116, v116
	v_add_f32_e32 v117, 1.0, v117
	v_mul_f32_e32 v108, 0xbfb8aa3b, v108
	v_pk_mul_f32 v[110:111], v[110:111], v[162:163] op_sel_hi:[1,0]
	v_mul_f32_e32 v109, 0xbfb8aa3b, v109
	v_cvt_u32_f32_sdwa v130, v130 dst_sel:WORD_1 dst_unused:UNUSED_PAD src0_sel:DWORD
	v_cvt_u32_f32_sdwa v126, v126 dst_sel:WORD_1 dst_unused:UNUSED_PAD src0_sel:DWORD
	v_cvt_u32_f32_sdwa v131, v131 dst_sel:BYTE_3 dst_unused:UNUSED_PAD src0_sel:DWORD
	v_cvt_u32_f32_sdwa v127, v127 dst_sel:BYTE_3 dst_unused:UNUSED_PAD src0_sel:DWORD
	v_add_f32_e32 v120, 1.0, v120
	v_add_f32_e32 v121, 1.0, v121
	v_rcp_f32_e32 v117, v117
	v_add_f32_e32 v118, 1.0, v118
	v_add_f32_e32 v119, 1.0, v119
	v_exp_f32_e32 v108, v108
	v_exp_f32_e32 v109, v109
	v_mul_f32_e32 v110, 0xbfb8aa3b, v110
	v_mul_f32_e32 v111, 0xbfb8aa3b, v111
	v_rcp_f32_e32 v120, v120
	v_rcp_f32_e32 v121, v121
	v_add_f32_e32 v122, 1.0, v122
	v_rcp_f32_e32 v118, v118
	v_add_f32_e32 v123, 1.0, v123
	v_rcp_f32_e32 v119, v119
	v_pk_mul_f32 v[112:113], v[112:113], v[162:163] op_sel_hi:[1,0]
	v_exp_f32_e32 v110, v110
	v_exp_f32_e32 v111, v111
	v_rcp_f32_e32 v122, v122
	v_rcp_f32_e32 v123, v123
	v_pk_mul_f32 v[114:115], v[114:115], v[162:163] op_sel_hi:[1,0]
	v_mul_f32_e32 v112, 0xbfb8aa3b, v112
	v_mul_f32_e32 v113, 0xbfb8aa3b, v113
	v_lshl_or_b32 v128, v129, 8, v128
	v_lshl_or_b32 v125, v125, 8, v124
	v_fma_f32 v116, v116, s39, 0.5
	v_exp_f32_e32 v112, v112
	v_exp_f32_e32 v113, v113
	v_mul_f32_e32 v114, 0xbfb8aa3b, v114
	v_mul_f32_e32 v115, 0xbfb8aa3b, v115
	v_or3_b32 v124, v128, v130, v131
;     template <int ACT, int AUX> __device__ __forceinline__ void run(const f32x4 (&acc)[2][2][4][2], const Unit& uu, int wr, int wc, int fr, int fq) const {
;     ...
;                 for (int bj = 0; bj < 2; ++bj) { f32x4 v0 = acc[ai][bj][m][0] * rs, v1 = acc[ai][bj][m][1] * rs;
; #pragma unroll
;                     for (int j = 0; j < 4; ++j) { v0[j] = act_f<ACT>(v0[j]); v1[j] = act_f<ACT>(v1[j]); }
;                     if (AUX == 4) {
;                         unsigned q[8];
; #pragma unroll
;                         for (int j = 0; j < 4; ++j) { q[j] = (unsigned)fminf(fmaxf(fmaf(v0[j], 255.0f, 0.5f), 1.0f), 255.0f); q[4 + j] = (unsigned)fminf(fmaxf(fmaf(v1[j], 255.0f, 0.5f), 1.0f), 255.0f); }
;                         u32x2 w8; w8.x = q[0] | (q[1] << 8) | (q[2] << 16) | (q[3] << 24); w8.y = q[4] | (q[5] << 8) | (q[6] << 16) | (q[7] << 24);
;                         __builtin_nontemporal_store(w8, (u32x2*)(g8 + ((size_t)((u.pn - 52) >> 4) * cfg::MT + r) * cfg::DM + ((u.pn - 52) & 15) * BM + wc * 32 + 8 * fq + bj * HALF));
	v_or3_b32 v125, v125, v126, v127
	v_med3_f32 v116, v116, 1.0, v231
	v_fma_f32 v117, v117, s39, 0.5
	v_add_f32_e32 v108, 1.0, v108
	v_add_f32_e32 v109, 1.0, v109
	v_exp_f32_e32 v114, v114
	v_exp_f32_e32 v115, v115
	global_store_dwordx2 v[148:149], v[124:125], off offset:-4096 nt
	v_fma_f32 v120, v120, s39, 0.5
	v_cvt_u32_f32_e32 v124, v116
	v_fma_f32 v116, v121, s39, 0.5
	v_med3_f32 v117, v117, 1.0, v231
	v_fma_f32 v118, v118, s39, 0.5
	v_fma_f32 v119, v119, s39, 0.5
	v_rcp_f32_e32 v108, v108
	v_rcp_f32_e32 v109, v109
	v_add_f32_e32 v110, 1.0, v110
	v_add_f32_e32 v111, 1.0, v111
	v_med3_f32 v120, v120, 1.0, v231
	v_med3_f32 v116, v116, 1.0, v231
	v_cvt_u32_f32_e32 v117, v117
	v_fma_f32 v121, v122, s39, 0.5
	v_med3_f32 v118, v118, 1.0, v231
	v_fma_f32 v122, v123, s39, 0.5
	v_med3_f32 v119, v119, 1.0, v231
	v_rcp_f32_e32 v110, v110
	v_rcp_f32_e32 v111, v111
	v_cvt_u32_f32_e32 v120, v120
	v_cvt_u32_f32_e32 v116, v116
	v_med3_f32 v121, v121, 1.0, v231
	v_cvt_u32_f32_sdwa v118, v118 dst_sel:WORD_1 dst_unused:UNUSED_PAD src0_sel:DWORD
	v_med3_f32 v122, v122, 1.0, v231
	v_cvt_u32_f32_sdwa v119, v119 dst_sel:BYTE_3 dst_unused:UNUSED_PAD src0_sel:DWORD
	v_add_f32_e32 v112, 1.0, v112
	v_add_f32_e32 v113, 1.0, v113
	v_pk_mul_f32 v[100:101], v[100:101], v[162:163] op_sel_hi:[1,0]
	v_cvt_u32_f32_sdwa v121, v121 dst_sel:WORD_1 dst_unused:UNUSED_PAD src0_sel:DWORD
	v_cvt_u32_f32_sdwa v122, v122 dst_sel:BYTE_3 dst_unused:UNUSED_PAD src0_sel:DWORD
	v_rcp_f32_e32 v112, v112
	v_rcp_f32_e32 v113, v113
	v_add_f32_e32 v114, 1.0, v114
	v_add_f32_e32 v115, 1.0, v115
	v_mul_f32_e32 v100, 0xbfb8aa3b, v100
	v_rsq_f32_e32 v160, v150
	v_rcp_f32_e32 v114, v114
	v_rcp_f32_e32 v115, v115
	v_fma_f32 v108, v108, s39, 0.5
	v_fma_f32 v109, v109, s39, 0.5
	v_pk_mul_f32 v[104:105], v[104:105], v[162:163] op_sel_hi:[1,0]
	v_exp_f32_e32 v100, v100
	v_pk_mul_f32 v[102:103], v[102:103], v[162:163] op_sel_hi:[1,0]
	v_mul_f32_e32 v101, 0xbfb8aa3b, v101
	v_lshl_or_b32 v117, v117, 8, v124
	v_med3_f32 v108, v108, 1.0, v231
	v_med3_f32 v109, v109, 1.0, v231
	v_fma_f32 v110, v110, s39, 0.5
	v_fma_f32 v111, v111, s39, 0.5
	v_pk_mul_f32 v[106:107], v[106:107], v[162:163] op_sel_hi:[1,0]
	v_mul_f32_e32 v104, 0xbfb8aa3b, v104
	v_mul_f32_e32 v105, 0xbfb8aa3b, v105
	v_exp_f32_e32 v101, v101
	v_mul_f32_e32 v102, 0xbfb8aa3b, v102
	v_mul_f32_e32 v103, 0xbfb8aa3b, v103
	v_lshl_or_b32 v116, v116, 8, v120
	v_or3_b32 v117, v117, v118, v119
	v_cvt_u32_f32_e32 v118, v108
	v_cvt_u32_f32_e32 v109, v109
	v_med3_f32 v110, v110, 1.0, v231
	v_med3_f32 v111, v111, 1.0, v231
	v_exp_f32_e32 v104, v104
	v_exp_f32_e32 v105, v105
	v_mul_f32_e32 v106, 0xbfb8aa3b, v106
	v_exp_f32_e32 v102, v102
	v_mul_f32_e32 v107, 0xbfb8aa3b, v107
	v_exp_f32_e32 v103, v103
	v_or3_b32 v116, v116, v121, v122
	v_fma_f32 v112, v112, s39, 0.5
	v_fma_f32 v108, v113, s39, 0.5
	v_cvt_u32_f32_sdwa v110, v110 dst_sel:WORD_1 dst_unused:UNUSED_PAD src0_sel:DWORD
	v_cvt_u32_f32_sdwa v111, v111 dst_sel:BYTE_3 dst_unused:UNUSED_PAD src0_sel:DWORD
	v_exp_f32_e32 v106, v106
	v_exp_f32_e32 v107, v107
	global_store_dwordx2 v[148:149], v[116:117], off offset:-3584 nt
	v_or_b32_e32 v116, 16, v156
	v_med3_f32 v112, v112, 1.0, v231
	v_med3_f32 v108, v108, 1.0, v231
	v_fma_f32 v113, v114, s39, 0.5
	v_fma_f32 v114, v115, s39, 0.5
	v_add_f32_e32 v100, 1.0, v100
	v_pk_mul_f32 v[92:93], v[92:93], v[160:161] op_sel_hi:[1,0]
	v_ashrrev_i32_e32 v117, 31, v116
	v_cvt_u32_f32_e32 v112, v112
	v_cvt_u32_f32_e32 v108, v108
	v_med3_f32 v113, v113, 1.0, v231
	v_med3_f32 v114, v114, 1.0, v231
	v_rcp_f32_e32 v100, v100
	v_add_f32_e32 v101, 1.0, v101
	v_mul_f32_e32 v92, 0xbfb8aa3b, v92
	v_pk_mul_f32 v[94:95], v[94:95], v[160:161] op_sel_hi:[1,0]
	v_mul_f32_e32 v93, 0xbfb8aa3b, v93
	v_lshlrev_b64 v[116:117], 12, v[116:117]
	v_cvt_u32_f32_sdwa v113, v113 dst_sel:WORD_1 dst_unused:UNUSED_PAD src0_sel:DWORD
	v_cvt_u32_f32_sdwa v114, v114 dst_sel:BYTE_3 dst_unused:UNUSED_PAD src0_sel:DWORD
	v_lshl_or_b32 v109, v109, 8, v118
	v_add_f32_e32 v104, 1.0, v104
	v_add_f32_e32 v105, 1.0, v105
	v_rcp_f32_e32 v101, v101
	v_add_f32_e32 v102, 1.0, v102
	v_add_f32_e32 v103, 1.0, v103
	v_exp_f32_e32 v92, v92
	v_exp_f32_e32 v93, v93
	v_mul_f32_e32 v94, 0xbfb8aa3b, v94
	v_mul_f32_e32 v95, 0xbfb8aa3b, v95
	v_or3_b32 v109, v109, v110, v111
	v_lshl_add_u64 v[110:111], s[12:13], 0, v[116:117]
	v_rcp_f32_e32 v104, v104
	v_rcp_f32_e32 v105, v105
	v_add_f32_e32 v106, 1.0, v106
	v_rcp_f32_e32 v102, v102
	v_add_f32_e32 v107, 1.0, v107
	v_rcp_f32_e32 v103, v103
	v_pk_mul_f32 v[96:97], v[96:97], v[160:161] op_sel_hi:[1,0]
	v_exp_f32_e32 v94, v94
	v_exp_f32_e32 v95, v95
	v_lshl_add_u64 v[110:111], v[110:111], 0, s[2:3]
	v_rcp_f32_e32 v106, v106
	v_rcp_f32_e32 v107, v107
	v_pk_mul_f32 v[98:99], v[98:99], v[160:161] op_sel_hi:[1,0]
	v_mul_f32_e32 v96, 0xbfb8aa3b, v96
	v_mul_f32_e32 v97, 0xbfb8aa3b, v97
	v_lshl_or_b32 v108, v108, 8, v112
	v_lshl_add_u64 v[110:111], v[110:111], 0, s[30:31]
	v_fma_f32 v100, v100, s39, 0.5
	v_exp_f32_e32 v96, v96
	v_exp_f32_e32 v97, v97
	v_mul_f32_e32 v98, 0xbfb8aa3b, v98
	v_mul_f32_e32 v99, 0xbfb8aa3b, v99
	v_or3_b32 v108, v108, v113, v114
	v_lshl_add_u64 v[110:111], v[110:111], 0, v[138:139]
	v_med3_f32 v100, v100, 1.0, v231
	v_fma_f32 v101, v101, s39, 0.5
	v_add_f32_e32 v92, 1.0, v92
	v_add_f32_e32 v93, 1.0, v93
	v_exp_f32_e32 v98, v98
	v_exp_f32_e32 v99, v99
	global_store_dwordx2 v[148:149], v[108:109], off offset:-3072 nt
	v_fma_f32 v104, v104, s39, 0.5
	v_cvt_u32_f32_e32 v108, v100
	v_fma_f32 v100, v105, s39, 0.5
	v_med3_f32 v101, v101, 1.0, v231
	v_fma_f32 v102, v102, s39, 0.5
	v_fma_f32 v103, v103, s39, 0.5
	v_rcp_f32_e32 v92, v92
	v_rcp_f32_e32 v93, v93
;     template <int ACT, int AUX> __device__ __forceinline__ void run(const f32x4 (&acc)[2][2][4][2], const Unit& uu, int wr, int wc, int fr, int fq) const {
;     ...
;                 for (int bj = 0; bj < 2; ++bj) { f32x4 v0 = acc[ai][bj][m][0] * rs, v1 = acc[ai][bj][m][1] * rs;
; #pragma unroll
;                     for (int j = 0; j < 4; ++j) { v0[j] = act_f<ACT>(v0[j]); v1[j] = act_f<ACT>(v1[j]); }
;                     if (AUX == 4) {
;                         unsigned q[8];
; #pragma unroll
;                         for (int j = 0; j < 4; ++j) { q[j] = (unsigned)fminf(fmaxf(fmaf(v0[j], 255.0f, 0.5f), 1.0f), 255.0f); q[4 + j] = (unsigned)fminf(fmaxf(fmaf(v1[j], 255.0f, 0.5f), 1.0f), 255.0f); }
;                         u32x2 w8; w8.x = q[0] | (q[1] << 8) | (q[2] << 16) | (q[3] << 24); w8.y = q[4] | (q[5] << 8) | (q[6] << 16) | (q[7] << 24);
;                         __builtin_nontemporal_store(w8, (u32x2*)(g8 + ((size_t)((u.pn - 52) >> 4) * cfg::MT + r) * cfg::DM + ((u.pn - 52) & 15) * BM + wc * 32 + 8 * fq + bj * HALF));
	v_add_f32_e32 v94, 1.0, v94
	v_add_f32_e32 v95, 1.0, v95
	v_med3_f32 v104, v104, 1.0, v231
	v_med3_f32 v100, v100, 1.0, v231
	v_cvt_u32_f32_e32 v101, v101
	v_fma_f32 v105, v106, s39, 0.5
	v_med3_f32 v102, v102, 1.0, v231
	v_fma_f32 v106, v107, s39, 0.5
	v_med3_f32 v103, v103, 1.0, v231
	v_rcp_f32_e32 v94, v94
	v_rcp_f32_e32 v95, v95
	v_cvt_u32_f32_e32 v104, v104
	v_cvt_u32_f32_e32 v100, v100
	v_med3_f32 v105, v105, 1.0, v231
	v_cvt_u32_f32_sdwa v102, v102 dst_sel:WORD_1 dst_unused:UNUSED_PAD src0_sel:DWORD
	v_med3_f32 v106, v106, 1.0, v231
	v_cvt_u32_f32_sdwa v103, v103 dst_sel:BYTE_3 dst_unused:UNUSED_PAD src0_sel:DWORD
	v_add_f32_e32 v96, 1.0, v96
	v_add_f32_e32 v97, 1.0, v97
	v_pk_mul_f32 v[84:85], v[84:85], v[160:161] op_sel_hi:[1,0]
	v_fmamk_f32 v151, v153, 0x39800000, v221
	v_cvt_u32_f32_sdwa v105, v105 dst_sel:WORD_1 dst_unused:UNUSED_PAD src0_sel:DWORD
	v_cvt_u32_f32_sdwa v106, v106 dst_sel:BYTE_3 dst_unused:UNUSED_PAD src0_sel:DWORD
	v_rcp_f32_e32 v96, v96
	v_rcp_f32_e32 v97, v97
	v_add_f32_e32 v98, 1.0, v98
	v_add_f32_e32 v99, 1.0, v99
	v_mul_f32_e32 v84, 0xbfb8aa3b, v84
	v_fmamk_f32 v153, v155, 0x39800000, v221
	v_fmamk_f32 v155, v158, 0x39800000, v221
	v_rsq_f32_e32 v158, v151
	v_rcp_f32_e32 v98, v98
	v_rcp_f32_e32 v99, v99
	v_fma_f32 v92, v92, s39, 0.5
	v_fma_f32 v93, v93, s39, 0.5
	v_pk_mul_f32 v[88:89], v[88:89], v[160:161] op_sel_hi:[1,0]
	v_exp_f32_e32 v84, v84
	v_pk_mul_f32 v[86:87], v[86:87], v[160:161] op_sel_hi:[1,0]
	v_mul_f32_e32 v85, 0xbfb8aa3b, v85
	v_lshl_or_b32 v101, v101, 8, v108
	v_med3_f32 v92, v92, 1.0, v231
	v_med3_f32 v93, v93, 1.0, v231
	v_fma_f32 v94, v94, s39, 0.5
	v_fma_f32 v95, v95, s39, 0.5
	v_pk_mul_f32 v[90:91], v[90:91], v[160:161] op_sel_hi:[1,0]
	v_mul_f32_e32 v88, 0xbfb8aa3b, v88
	v_mul_f32_e32 v89, 0xbfb8aa3b, v89
	v_exp_f32_e32 v85, v85
	v_mul_f32_e32 v86, 0xbfb8aa3b, v86
	v_mul_f32_e32 v87, 0xbfb8aa3b, v87
	v_lshl_or_b32 v100, v100, 8, v104
	v_or3_b32 v101, v101, v102, v103
	v_cvt_u32_f32_e32 v102, v92
	v_cvt_u32_f32_e32 v93, v93
	v_med3_f32 v94, v94, 1.0, v231
	v_med3_f32 v95, v95, 1.0, v231
	v_exp_f32_e32 v88, v88
	v_exp_f32_e32 v89, v89
	v_mul_f32_e32 v90, 0xbfb8aa3b, v90
	v_exp_f32_e32 v86, v86
	v_mul_f32_e32 v91, 0xbfb8aa3b, v91
	v_exp_f32_e32 v87, v87
	v_or3_b32 v100, v100, v105, v106
	v_fma_f32 v96, v96, s39, 0.5
	v_fma_f32 v92, v97, s39, 0.5
	v_cvt_u32_f32_sdwa v94, v94 dst_sel:WORD_1 dst_unused:UNUSED_PAD src0_sel:DWORD
	v_cvt_u32_f32_sdwa v95, v95 dst_sel:BYTE_3 dst_unused:UNUSED_PAD src0_sel:DWORD
	v_exp_f32_e32 v90, v90
	v_exp_f32_e32 v91, v91
	global_store_dwordx2 v[148:149], v[100:101], off offset:-2560 nt
	v_or_b32_e32 v100, 32, v156
	v_med3_f32 v96, v96, 1.0, v231
	v_med3_f32 v92, v92, 1.0, v231
	v_fma_f32 v97, v98, s39, 0.5
	v_fma_f32 v98, v99, s39, 0.5
	v_add_f32_e32 v84, 1.0, v84
	v_pk_mul_f32 v[76:77], v[76:77], v[158:159] op_sel_hi:[1,0]
	v_ashrrev_i32_e32 v101, 31, v100
	v_cvt_u32_f32_e32 v96, v96
	v_cvt_u32_f32_e32 v92, v92
	v_med3_f32 v97, v97, 1.0, v231
	v_med3_f32 v98, v98, 1.0, v231
	v_rcp_f32_e32 v84, v84
	v_add_f32_e32 v85, 1.0, v85
	v_mul_f32_e32 v76, 0xbfb8aa3b, v76
	v_pk_mul_f32 v[78:79], v[78:79], v[158:159] op_sel_hi:[1,0]
	v_mul_f32_e32 v77, 0xbfb8aa3b, v77
	v_lshlrev_b64 v[100:101], 12, v[100:101]
	v_cvt_u32_f32_sdwa v97, v97 dst_sel:WORD_1 dst_unused:UNUSED_PAD src0_sel:DWORD
	v_cvt_u32_f32_sdwa v98, v98 dst_sel:BYTE_3 dst_unused:UNUSED_PAD src0_sel:DWORD
	v_lshl_or_b32 v93, v93, 8, v102
	v_add_f32_e32 v88, 1.0, v88
	v_add_f32_e32 v89, 1.0, v89
	v_rcp_f32_e32 v85, v85
	v_add_f32_e32 v86, 1.0, v86
	v_add_f32_e32 v87, 1.0, v87
	v_exp_f32_e32 v76, v76
	v_exp_f32_e32 v77, v77
	v_mul_f32_e32 v78, 0xbfb8aa3b, v78
	v_mul_f32_e32 v79, 0xbfb8aa3b, v79
	v_or3_b32 v93, v93, v94, v95
	v_lshl_add_u64 v[94:95], s[12:13], 0, v[100:101]
	v_rcp_f32_e32 v88, v88
	v_rcp_f32_e32 v89, v89
	v_add_f32_e32 v90, 1.0, v90
	v_rcp_f32_e32 v86, v86
	v_add_f32_e32 v91, 1.0, v91
	v_rcp_f32_e32 v87, v87
	v_pk_mul_f32 v[80:81], v[80:81], v[158:159] op_sel_hi:[1,0]
	v_exp_f32_e32 v78, v78
	v_exp_f32_e32 v79, v79
	v_lshl_add_u64 v[94:95], v[94:95], 0, s[2:3]
	v_rcp_f32_e32 v90, v90
	v_rcp_f32_e32 v91, v91
	v_pk_mul_f32 v[82:83], v[82:83], v[158:159] op_sel_hi:[1,0]
	v_mul_f32_e32 v80, 0xbfb8aa3b, v80
	v_mul_f32_e32 v81, 0xbfb8aa3b, v81
	v_lshl_or_b32 v92, v92, 8, v96
	v_lshl_add_u64 v[94:95], v[94:95], 0, s[30:31]
	v_fma_f32 v84, v84, s39, 0.5
	v_exp_f32_e32 v80, v80
	v_exp_f32_e32 v81, v81
	v_mul_f32_e32 v82, 0xbfb8aa3b, v82
	v_mul_f32_e32 v83, 0xbfb8aa3b, v83
	v_or3_b32 v92, v92, v97, v98
	v_lshl_add_u64 v[94:95], v[94:95], 0, v[138:139]
	v_med3_f32 v84, v84, 1.0, v231
	v_fma_f32 v85, v85, s39, 0.5
	v_add_f32_e32 v76, 1.0, v76
	v_add_f32_e32 v77, 1.0, v77
	v_exp_f32_e32 v82, v82
	v_exp_f32_e32 v83, v83
	global_store_dwordx2 v[148:149], v[92:93], off offset:-2048 nt
	v_fma_f32 v88, v88, s39, 0.5
	v_cvt_u32_f32_e32 v92, v84
	v_fma_f32 v84, v89, s39, 0.5
	v_med3_f32 v85, v85, 1.0, v231
	v_fma_f32 v86, v86, s39, 0.5
	v_fma_f32 v87, v87, s39, 0.5
	v_rcp_f32_e32 v76, v76
	v_rcp_f32_e32 v77, v77
	v_add_f32_e32 v78, 1.0, v78
	v_add_f32_e32 v79, 1.0, v79
	v_med3_f32 v88, v88, 1.0, v231
	v_med3_f32 v84, v84, 1.0, v231
	v_cvt_u32_f32_e32 v85, v85
	v_fma_f32 v89, v90, s39, 0.5
	v_med3_f32 v86, v86, 1.0, v231
	v_fma_f32 v90, v91, s39, 0.5
	v_med3_f32 v87, v87, 1.0, v231
	v_rcp_f32_e32 v78, v78
	v_rcp_f32_e32 v79, v79
	v_cvt_u32_f32_e32 v88, v88
	v_cvt_u32_f32_e32 v84, v84
	v_med3_f32 v89, v89, 1.0, v231
	v_cvt_u32_f32_sdwa v86, v86 dst_sel:WORD_1 dst_unused:UNUSED_PAD src0_sel:DWORD
	v_med3_f32 v90, v90, 1.0, v231
	v_cvt_u32_f32_sdwa v87, v87 dst_sel:BYTE_3 dst_unused:UNUSED_PAD src0_sel:DWORD
;     template <int ACT, int AUX> __device__ __forceinline__ void run(const f32x4 (&acc)[2][2][4][2], const Unit& uu, int wr, int wc, int fr, int fq) const {
;     ...
;                 for (int bj = 0; bj < 2; ++bj) { f32x4 v0 = acc[ai][bj][m][0] * rs, v1 = acc[ai][bj][m][1] * rs;
; #pragma unroll
;                     for (int j = 0; j < 4; ++j) { v0[j] = act_f<ACT>(v0[j]); v1[j] = act_f<ACT>(v1[j]); }
;                     if (AUX == 4) {
;                         unsigned q[8];
; #pragma unroll
;                         for (int j = 0; j < 4; ++j) { q[j] = (unsigned)fminf(fmaxf(fmaf(v0[j], 255.0f, 0.5f), 1.0f), 255.0f); q[4 + j] = (unsigned)fminf(fmaxf(fmaf(v1[j], 255.0f, 0.5f), 1.0f), 255.0f); }
;                         u32x2 w8; w8.x = q[0] | (q[1] << 8) | (q[2] << 16) | (q[3] << 24); w8.y = q[4] | (q[5] << 8) | (q[6] << 16) | (q[7] << 24);
;                         __builtin_nontemporal_store(w8, (u32x2*)(g8 + ((size_t)((u.pn - 52) >> 4) * cfg::MT + r) * cfg::DM + ((u.pn - 52) & 15) * BM + wc * 32 + 8 * fq + bj * HALF));
	v_add_f32_e32 v80, 1.0, v80
	v_add_f32_e32 v81, 1.0, v81
	v_pk_mul_f32 v[68:69], v[68:69], v[158:159] op_sel_hi:[1,0]
	v_cvt_u32_f32_sdwa v89, v89 dst_sel:WORD_1 dst_unused:UNUSED_PAD src0_sel:DWORD
	v_cvt_u32_f32_sdwa v90, v90 dst_sel:BYTE_3 dst_unused:UNUSED_PAD src0_sel:DWORD
	v_rcp_f32_e32 v80, v80
	v_rcp_f32_e32 v81, v81
	v_add_f32_e32 v82, 1.0, v82
	v_add_f32_e32 v83, 1.0, v83
	v_mul_f32_e32 v68, 0xbfb8aa3b, v68
	v_rcp_f32_e32 v82, v82
	v_rcp_f32_e32 v83, v83
	v_fma_f32 v76, v76, s39, 0.5
	v_fma_f32 v77, v77, s39, 0.5
	v_pk_mul_f32 v[72:73], v[72:73], v[158:159] op_sel_hi:[1,0]
	v_exp_f32_e32 v68, v68
	v_fmamk_f32 v152, v154, 0x39800000, v221
	v_lshl_or_b32 v85, v85, 8, v92
	v_med3_f32 v76, v76, 1.0, v231
	v_med3_f32 v77, v77, 1.0, v231
	v_fma_f32 v78, v78, s39, 0.5
	v_fma_f32 v79, v79, s39, 0.5
	v_pk_mul_f32 v[74:75], v[74:75], v[158:159] op_sel_hi:[1,0]
	v_mul_f32_e32 v72, 0xbfb8aa3b, v72
	v_pk_mul_f32 v[70:71], v[70:71], v[158:159] op_sel_hi:[1,0]
	v_mul_f32_e32 v73, 0xbfb8aa3b, v73
	v_mul_f32_e32 v69, 0xbfb8aa3b, v69
	v_rsq_f32_e32 v154, v152
	v_lshl_or_b32 v84, v84, 8, v88
	v_or3_b32 v85, v85, v86, v87
	v_cvt_u32_f32_e32 v86, v76
	v_cvt_u32_f32_e32 v77, v77
	v_med3_f32 v78, v78, 1.0, v231
	v_med3_f32 v79, v79, 1.0, v231
	v_exp_f32_e32 v72, v72
	v_exp_f32_e32 v73, v73
	v_exp_f32_e32 v69, v69
	v_mul_f32_e32 v74, 0xbfb8aa3b, v74
	v_mul_f32_e32 v70, 0xbfb8aa3b, v70
	v_mul_f32_e32 v75, 0xbfb8aa3b, v75
	v_mul_f32_e32 v71, 0xbfb8aa3b, v71
	v_or3_b32 v84, v84, v89, v90
	v_fma_f32 v80, v80, s39, 0.5
	v_fma_f32 v76, v81, s39, 0.5
	v_cvt_u32_f32_sdwa v78, v78 dst_sel:WORD_1 dst_unused:UNUSED_PAD src0_sel:DWORD
	v_cvt_u32_f32_sdwa v79, v79 dst_sel:BYTE_3 dst_unused:UNUSED_PAD src0_sel:DWORD
	v_exp_f32_e32 v74, v74
	v_exp_f32_e32 v70, v70
	v_exp_f32_e32 v75, v75
	v_exp_f32_e32 v71, v71
	global_store_dwordx2 v[148:149], v[84:85], off offset:-1536 nt
	v_or_b32_e32 v84, 48, v156
	v_med3_f32 v80, v80, 1.0, v231
	v_med3_f32 v76, v76, 1.0, v231
	v_fma_f32 v81, v82, s39, 0.5
	v_fma_f32 v82, v83, s39, 0.5
	v_add_f32_e32 v68, 1.0, v68
	v_ashrrev_i32_e32 v85, 31, v84
	v_cvt_u32_f32_e32 v80, v80
	v_cvt_u32_f32_e32 v76, v76
	v_med3_f32 v81, v81, 1.0, v231
	v_med3_f32 v82, v82, 1.0, v231
	v_rcp_f32_e32 v68, v68
	v_lshlrev_b64 v[84:85], 12, v[84:85]
	v_cvt_u32_f32_sdwa v81, v81 dst_sel:WORD_1 dst_unused:UNUSED_PAD src0_sel:DWORD
	v_cvt_u32_f32_sdwa v82, v82 dst_sel:BYTE_3 dst_unused:UNUSED_PAD src0_sel:DWORD
	v_lshl_or_b32 v77, v77, 8, v86
	v_add_f32_e32 v72, 1.0, v72
	v_add_f32_e32 v73, 1.0, v73
	v_add_f32_e32 v69, 1.0, v69
	v_pk_mul_f32 v[60:61], v[60:61], v[154:155] op_sel_hi:[1,0]
	v_or3_b32 v77, v77, v78, v79
	v_lshl_add_u64 v[78:79], s[12:13], 0, v[84:85]
	v_rcp_f32_e32 v72, v72
	v_rcp_f32_e32 v73, v73
	v_rcp_f32_e32 v69, v69
	v_add_f32_e32 v74, 1.0, v74
	v_add_f32_e32 v70, 1.0, v70
	v_add_f32_e32 v75, 1.0, v75
	v_add_f32_e32 v71, 1.0, v71
	v_mul_f32_e32 v60, 0xbfb8aa3b, v60
	v_lshl_add_u64 v[78:79], v[78:79], 0, s[2:3]
	v_rcp_f32_e32 v74, v74
	v_rcp_f32_e32 v70, v70
	v_rcp_f32_e32 v75, v75
	v_rcp_f32_e32 v71, v71
	v_pk_mul_f32 v[64:65], v[64:65], v[154:155] op_sel_hi:[1,0]
	v_exp_f32_e32 v60, v60
	v_lshl_or_b32 v76, v76, 8, v80
	v_lshl_add_u64 v[78:79], v[78:79], 0, s[30:31]
	v_fma_f32 v68, v68, s39, 0.5
	v_pk_mul_f32 v[66:67], v[66:67], v[154:155] op_sel_hi:[1,0]
	v_mul_f32_e32 v64, 0xbfb8aa3b, v64
	v_pk_mul_f32 v[62:63], v[62:63], v[154:155] op_sel_hi:[1,0]
	v_mul_f32_e32 v65, 0xbfb8aa3b, v65
	v_mul_f32_e32 v61, 0xbfb8aa3b, v61
	v_or3_b32 v76, v76, v81, v82
	v_lshl_add_u64 v[78:79], v[78:79], 0, v[138:139]
	v_med3_f32 v68, v68, 1.0, v231
	v_exp_f32_e32 v64, v64
	v_exp_f32_e32 v65, v65
	v_exp_f32_e32 v61, v61
	v_mul_f32_e32 v66, 0xbfb8aa3b, v66
	v_mul_f32_e32 v62, 0xbfb8aa3b, v62
	v_mul_f32_e32 v67, 0xbfb8aa3b, v67
	v_mul_f32_e32 v63, 0xbfb8aa3b, v63
	global_store_dwordx2 v[148:149], v[76:77], off offset:-1024 nt
	v_fma_f32 v72, v72, s39, 0.5
	v_cvt_u32_f32_e32 v76, v68
	v_fma_f32 v68, v73, s39, 0.5
	v_fma_f32 v69, v69, s39, 0.5
	v_exp_f32_e32 v66, v66
	v_exp_f32_e32 v62, v62
	v_exp_f32_e32 v67, v67
	v_exp_f32_e32 v63, v63
	v_med3_f32 v72, v72, 1.0, v231
	v_med3_f32 v68, v68, 1.0, v231
	v_med3_f32 v69, v69, 1.0, v231
	v_fma_f32 v73, v74, s39, 0.5
	v_fma_f32 v70, v70, s39, 0.5
	v_fma_f32 v74, v75, s39, 0.5
	v_fma_f32 v71, v71, s39, 0.5
	v_add_f32_e32 v60, 1.0, v60
	v_cvt_u32_f32_e32 v72, v72
	v_cvt_u32_f32_e32 v68, v68
	v_cvt_u32_f32_e32 v69, v69
	v_med3_f32 v73, v73, 1.0, v231
	v_med3_f32 v70, v70, 1.0, v231
	v_med3_f32 v74, v74, 1.0, v231
	v_med3_f32 v71, v71, 1.0, v231
	v_rcp_f32_e32 v60, v60
	v_cvt_u32_f32_sdwa v73, v73 dst_sel:WORD_1 dst_unused:UNUSED_PAD src0_sel:DWORD
	v_cvt_u32_f32_sdwa v70, v70 dst_sel:WORD_1 dst_unused:UNUSED_PAD src0_sel:DWORD
	v_cvt_u32_f32_sdwa v74, v74 dst_sel:BYTE_3 dst_unused:UNUSED_PAD src0_sel:DWORD
	v_cvt_u32_f32_sdwa v71, v71 dst_sel:BYTE_3 dst_unused:UNUSED_PAD src0_sel:DWORD
	v_add_f32_e32 v64, 1.0, v64
	v_add_f32_e32 v65, 1.0, v65
	v_add_f32_e32 v61, 1.0, v61
	v_pk_mul_f32 v[52:53], v[52:53], v[154:155] op_sel_hi:[1,0]
	v_rcp_f32_e32 v64, v64
	v_rcp_f32_e32 v65, v65
	v_rcp_f32_e32 v61, v61
	v_add_f32_e32 v66, 1.0, v66
	v_add_f32_e32 v62, 1.0, v62
	v_add_f32_e32 v67, 1.0, v67
	v_add_f32_e32 v63, 1.0, v63
	v_mul_f32_e32 v52, 0xbfb8aa3b, v52
	v_rcp_f32_e32 v66, v66
	v_rcp_f32_e32 v62, v62
	v_rcp_f32_e32 v67, v67
	v_rcp_f32_e32 v63, v63
	v_pk_mul_f32 v[56:57], v[56:57], v[154:155] op_sel_hi:[1,0]
	v_exp_f32_e32 v52, v52
	v_lshl_or_b32 v68, v68, 8, v72
	v_lshl_or_b32 v69, v69, 8, v76
	v_fma_f32 v60, v60, s39, 0.5
	v_pk_mul_f32 v[58:59], v[58:59], v[154:155] op_sel_hi:[1,0]
	v_mul_f32_e32 v56, 0xbfb8aa3b, v56
;     template <int ACT, int AUX> __device__ __forceinline__ void run(const f32x4 (&acc)[2][2][4][2], const Unit& uu, int wr, int wc, int fr, int fq) const {
;     ...
;                 for (int bj = 0; bj < 2; ++bj) { f32x4 v0 = acc[ai][bj][m][0] * rs, v1 = acc[ai][bj][m][1] * rs;
; #pragma unroll
;                     for (int j = 0; j < 4; ++j) { v0[j] = act_f<ACT>(v0[j]); v1[j] = act_f<ACT>(v1[j]); }
;                     if (AUX == 4) {
;                         unsigned q[8];
; #pragma unroll
;                         for (int j = 0; j < 4; ++j) { q[j] = (unsigned)fminf(fmaxf(fmaf(v0[j], 255.0f, 0.5f), 1.0f), 255.0f); q[4 + j] = (unsigned)fminf(fmaxf(fmaf(v1[j], 255.0f, 0.5f), 1.0f), 255.0f); }
;                         u32x2 w8; w8.x = q[0] | (q[1] << 8) | (q[2] << 16) | (q[3] << 24); w8.y = q[4] | (q[5] << 8) | (q[6] << 16) | (q[7] << 24);
;                         __builtin_nontemporal_store(w8, (u32x2*)(g8 + ((size_t)((u.pn - 52) >> 4) * cfg::MT + r) * cfg::DM + ((u.pn - 52) & 15) * BM + wc * 32 + 8 * fq + bj * HALF));
	v_pk_mul_f32 v[54:55], v[54:55], v[154:155] op_sel_hi:[1,0]
	v_mul_f32_e32 v57, 0xbfb8aa3b, v57
	v_mul_f32_e32 v53, 0xbfb8aa3b, v53
	v_rsq_f32_e32 v152, v153
	v_or3_b32 v68, v68, v73, v74
	v_or3_b32 v69, v69, v70, v71
	v_med3_f32 v60, v60, 1.0, v231
	v_exp_f32_e32 v56, v56
	v_exp_f32_e32 v57, v57
	v_exp_f32_e32 v53, v53
	v_mul_f32_e32 v58, 0xbfb8aa3b, v58
	v_mul_f32_e32 v54, 0xbfb8aa3b, v54
	v_mul_f32_e32 v59, 0xbfb8aa3b, v59
	v_mul_f32_e32 v55, 0xbfb8aa3b, v55
	global_store_dwordx2 v[148:149], v[68:69], off offset:-512 nt
	v_fma_f32 v64, v64, s39, 0.5
	v_cvt_u32_f32_e32 v68, v60
	v_fma_f32 v60, v65, s39, 0.5
	v_fma_f32 v61, v61, s39, 0.5
	v_exp_f32_e32 v58, v58
	v_exp_f32_e32 v54, v54
	v_exp_f32_e32 v59, v59
	v_exp_f32_e32 v55, v55
	v_med3_f32 v64, v64, 1.0, v231
	v_med3_f32 v60, v60, 1.0, v231
	v_med3_f32 v61, v61, 1.0, v231
	v_fma_f32 v65, v66, s39, 0.5
	v_fma_f32 v62, v62, s39, 0.5
	v_fma_f32 v66, v67, s39, 0.5
	v_fma_f32 v63, v63, s39, 0.5
	v_add_f32_e32 v52, 1.0, v52
	v_cvt_u32_f32_e32 v64, v64
	v_cvt_u32_f32_e32 v60, v60
	v_cvt_u32_f32_e32 v61, v61
	v_med3_f32 v65, v65, 1.0, v231
	v_med3_f32 v62, v62, 1.0, v231
	v_med3_f32 v66, v66, 1.0, v231
	v_med3_f32 v63, v63, 1.0, v231
	v_rcp_f32_e32 v52, v52
	v_cvt_u32_f32_sdwa v65, v65 dst_sel:WORD_1 dst_unused:UNUSED_PAD src0_sel:DWORD
	v_cvt_u32_f32_sdwa v62, v62 dst_sel:WORD_1 dst_unused:UNUSED_PAD src0_sel:DWORD
	v_cvt_u32_f32_sdwa v66, v66 dst_sel:BYTE_3 dst_unused:UNUSED_PAD src0_sel:DWORD
	v_cvt_u32_f32_sdwa v63, v63 dst_sel:BYTE_3 dst_unused:UNUSED_PAD src0_sel:DWORD
	v_add_f32_e32 v56, 1.0, v56
	v_add_f32_e32 v57, 1.0, v57
	v_add_f32_e32 v53, 1.0, v53
	v_pk_mul_f32 v[44:45], v[44:45], v[152:153] op_sel_hi:[1,0]
	v_rcp_f32_e32 v56, v56
	v_rcp_f32_e32 v57, v57
	v_rcp_f32_e32 v53, v53
	v_add_f32_e32 v58, 1.0, v58
	v_add_f32_e32 v54, 1.0, v54
	v_add_f32_e32 v59, 1.0, v59
	v_add_f32_e32 v55, 1.0, v55
	v_mul_f32_e32 v44, 0xbfb8aa3b, v44
	s_mov_b32 s2, 0x80000
	v_rcp_f32_e32 v58, v58
	v_rcp_f32_e32 v54, v54
	v_rcp_f32_e32 v59, v59
	v_rcp_f32_e32 v55, v55
	v_pk_mul_f32 v[48:49], v[48:49], v[152:153] op_sel_hi:[1,0]
	v_exp_f32_e32 v44, v44
	v_lshl_or_b32 v60, v60, 8, v64
	v_lshl_or_b32 v61, v61, 8, v68
	v_add_co_u32_e32 v64, vcc, s2, v148
	v_fma_f32 v52, v52, s39, 0.5
	v_pk_mul_f32 v[50:51], v[50:51], v[152:153] op_sel_hi:[1,0]
	v_mul_f32_e32 v48, 0xbfb8aa3b, v48
	v_pk_mul_f32 v[46:47], v[46:47], v[152:153] op_sel_hi:[1,0]
	v_mul_f32_e32 v49, 0xbfb8aa3b, v49
	v_mul_f32_e32 v45, 0xbfb8aa3b, v45
	v_or3_b32 v60, v60, v65, v66
	v_or3_b32 v61, v61, v62, v63
	v_addc_co_u32_e32 v65, vcc, 0, v149, vcc
	v_med3_f32 v52, v52, 1.0, v231
	v_exp_f32_e32 v48, v48
	v_exp_f32_e32 v49, v49
	v_exp_f32_e32 v45, v45
	v_mul_f32_e32 v50, 0xbfb8aa3b, v50
	v_mul_f32_e32 v46, 0xbfb8aa3b, v46
	v_mul_f32_e32 v51, 0xbfb8aa3b, v51
	v_mul_f32_e32 v47, 0xbfb8aa3b, v47
	global_store_dwordx2 v[148:149], v[60:61], off nt
	v_fma_f32 v56, v56, s39, 0.5
	v_cvt_u32_f32_e32 v60, v52
	v_fma_f32 v52, v57, s39, 0.5
	v_fma_f32 v53, v53, s39, 0.5
	v_exp_f32_e32 v50, v50
	v_exp_f32_e32 v46, v46
	v_exp_f32_e32 v51, v51
	v_exp_f32_e32 v47, v47
	v_med3_f32 v56, v56, 1.0, v231
	v_med3_f32 v52, v52, 1.0, v231
	v_med3_f32 v53, v53, 1.0, v231
	v_fma_f32 v57, v58, s39, 0.5
	v_fma_f32 v54, v54, s39, 0.5
	v_fma_f32 v58, v59, s39, 0.5
	v_fma_f32 v55, v55, s39, 0.5
	v_add_f32_e32 v44, 1.0, v44
	v_cvt_u32_f32_e32 v56, v56
	v_cvt_u32_f32_e32 v52, v52
	v_cvt_u32_f32_e32 v53, v53
	v_med3_f32 v57, v57, 1.0, v231
	v_med3_f32 v54, v54, 1.0, v231
	v_med3_f32 v58, v58, 1.0, v231
	v_med3_f32 v55, v55, 1.0, v231
	v_rcp_f32_e32 v44, v44
	v_cvt_u32_f32_sdwa v57, v57 dst_sel:WORD_1 dst_unused:UNUSED_PAD src0_sel:DWORD
	v_cvt_u32_f32_sdwa v54, v54 dst_sel:WORD_1 dst_unused:UNUSED_PAD src0_sel:DWORD
	v_cvt_u32_f32_sdwa v58, v58 dst_sel:BYTE_3 dst_unused:UNUSED_PAD src0_sel:DWORD
	v_cvt_u32_f32_sdwa v55, v55 dst_sel:BYTE_3 dst_unused:UNUSED_PAD src0_sel:DWORD
	v_add_f32_e32 v48, 1.0, v48
	v_add_f32_e32 v49, 1.0, v49
	v_add_f32_e32 v45, 1.0, v45
	v_pk_mul_f32 v[36:37], v[36:37], v[152:153] op_sel_hi:[1,0]
	v_rcp_f32_e32 v48, v48
	v_rcp_f32_e32 v49, v49
	v_rcp_f32_e32 v45, v45
	v_add_f32_e32 v50, 1.0, v50
	v_add_f32_e32 v46, 1.0, v46
	v_add_f32_e32 v51, 1.0, v51
	v_add_f32_e32 v47, 1.0, v47
	v_mul_f32_e32 v36, 0xbfb8aa3b, v36
	v_rcp_f32_e32 v50, v50
	v_rcp_f32_e32 v46, v46
	v_rcp_f32_e32 v51, v51
	v_rcp_f32_e32 v47, v47
	v_pk_mul_f32 v[40:41], v[40:41], v[152:153] op_sel_hi:[1,0]
	v_exp_f32_e32 v36, v36
	s_mov_b64 s[12:13], 0x80000
	v_lshl_or_b32 v52, v52, 8, v56
	v_lshl_or_b32 v53, v53, 8, v60
	v_fma_f32 v44, v44, s39, 0.5
	v_pk_mul_f32 v[42:43], v[42:43], v[152:153] op_sel_hi:[1,0]
	v_mul_f32_e32 v40, 0xbfb8aa3b, v40
	v_pk_mul_f32 v[38:39], v[38:39], v[152:153] op_sel_hi:[1,0]
	v_mul_f32_e32 v41, 0xbfb8aa3b, v41
	v_mul_f32_e32 v37, 0xbfb8aa3b, v37
	v_rsq_f32_e32 v150, v155
	v_lshl_add_u64 v[62:63], v[148:149], 0, s[12:13]
	v_or3_b32 v52, v52, v57, v58
	v_or3_b32 v53, v53, v54, v55
	v_med3_f32 v44, v44, 1.0, v231
	v_exp_f32_e32 v40, v40
	v_exp_f32_e32 v41, v41
	v_exp_f32_e32 v37, v37
	v_mul_f32_e32 v42, 0xbfb8aa3b, v42
	v_mul_f32_e32 v38, 0xbfb8aa3b, v38
	v_mul_f32_e32 v43, 0xbfb8aa3b, v43
	v_mul_f32_e32 v39, 0xbfb8aa3b, v39
	global_store_dwordx2 v[148:149], v[52:53], off offset:512 nt
	v_fma_f32 v48, v48, s39, 0.5
	v_cvt_u32_f32_e32 v52, v44
	v_fma_f32 v44, v49, s39, 0.5
	v_fma_f32 v45, v45, s39, 0.5
	v_exp_f32_e32 v42, v42
	v_exp_f32_e32 v38, v38
	v_exp_f32_e32 v43, v43
	v_exp_f32_e32 v39, v39
	v_med3_f32 v48, v48, 1.0, v231
	v_med3_f32 v44, v44, 1.0, v231
	v_med3_f32 v45, v45, 1.0, v231
	v_fma_f32 v49, v50, s39, 0.5
	v_fma_f32 v46, v46, s39, 0.5
;     template <int ACT, int AUX> __device__ __forceinline__ void run(const f32x4 (&acc)[2][2][4][2], const Unit& uu, int wr, int wc, int fr, int fq) const {
;     ...
;                 for (int bj = 0; bj < 2; ++bj) { f32x4 v0 = acc[ai][bj][m][0] * rs, v1 = acc[ai][bj][m][1] * rs;
; #pragma unroll
;                     for (int j = 0; j < 4; ++j) { v0[j] = act_f<ACT>(v0[j]); v1[j] = act_f<ACT>(v1[j]); }
;                     if (AUX == 4) {
;                         unsigned q[8];
; #pragma unroll
;                         for (int j = 0; j < 4; ++j) { q[j] = (unsigned)fminf(fmaxf(fmaf(v0[j], 255.0f, 0.5f), 1.0f), 255.0f); q[4 + j] = (unsigned)fminf(fmaxf(fmaf(v1[j], 255.0f, 0.5f), 1.0f), 255.0f); }
;                         u32x2 w8; w8.x = q[0] | (q[1] << 8) | (q[2] << 16) | (q[3] << 24); w8.y = q[4] | (q[5] << 8) | (q[6] << 16) | (q[7] << 24);
;                         __builtin_nontemporal_store(w8, (u32x2*)(g8 + ((size_t)((u.pn - 52) >> 4) * cfg::MT + r) * cfg::DM + ((u.pn - 52) & 15) * BM + wc * 32 + 8 * fq + bj * HALF));
	v_fma_f32 v50, v51, s39, 0.5
	v_fma_f32 v47, v47, s39, 0.5
	v_add_f32_e32 v36, 1.0, v36
	v_cvt_u32_f32_e32 v48, v48
	v_cvt_u32_f32_e32 v44, v44
	v_cvt_u32_f32_e32 v45, v45
	v_med3_f32 v49, v49, 1.0, v231
	v_med3_f32 v46, v46, 1.0, v231
	v_med3_f32 v50, v50, 1.0, v231
	v_med3_f32 v47, v47, 1.0, v231
	v_rcp_f32_e32 v36, v36
	v_cvt_u32_f32_sdwa v49, v49 dst_sel:WORD_1 dst_unused:UNUSED_PAD src0_sel:DWORD
	v_cvt_u32_f32_sdwa v46, v46 dst_sel:WORD_1 dst_unused:UNUSED_PAD src0_sel:DWORD
	v_cvt_u32_f32_sdwa v50, v50 dst_sel:BYTE_3 dst_unused:UNUSED_PAD src0_sel:DWORD
	v_cvt_u32_f32_sdwa v47, v47 dst_sel:BYTE_3 dst_unused:UNUSED_PAD src0_sel:DWORD
	v_add_f32_e32 v40, 1.0, v40
	v_add_f32_e32 v41, 1.0, v41
	v_add_f32_e32 v37, 1.0, v37
	v_pk_mul_f32 v[28:29], v[28:29], v[150:151] op_sel_hi:[1,0]
	v_rcp_f32_e32 v40, v40
	v_rcp_f32_e32 v41, v41
	v_rcp_f32_e32 v37, v37
	v_add_f32_e32 v42, 1.0, v42
	v_add_f32_e32 v38, 1.0, v38
	v_add_f32_e32 v43, 1.0, v43
	v_add_f32_e32 v39, 1.0, v39
	v_mul_f32_e32 v28, 0xbfb8aa3b, v28
	s_mov_b32 s2, 0x90000
	v_rcp_f32_e32 v42, v42
	v_rcp_f32_e32 v38, v38
	v_rcp_f32_e32 v43, v43
	v_rcp_f32_e32 v39, v39
	v_pk_mul_f32 v[32:33], v[32:33], v[150:151] op_sel_hi:[1,0]
	v_exp_f32_e32 v28, v28
	v_lshl_or_b32 v44, v44, 8, v48
	v_lshl_or_b32 v45, v45, 8, v52
	v_add_co_u32_e32 v48, vcc, s2, v148
	v_fma_f32 v36, v36, s39, 0.5
	v_pk_mul_f32 v[34:35], v[34:35], v[150:151] op_sel_hi:[1,0]
	v_mul_f32_e32 v32, 0xbfb8aa3b, v32
	v_pk_mul_f32 v[30:31], v[30:31], v[150:151] op_sel_hi:[1,0]
	v_mul_f32_e32 v33, 0xbfb8aa3b, v33
	v_mul_f32_e32 v29, 0xbfb8aa3b, v29
	v_or3_b32 v44, v44, v49, v50
	v_or3_b32 v45, v45, v46, v47
	v_addc_co_u32_e32 v49, vcc, 0, v149, vcc
	v_med3_f32 v36, v36, 1.0, v231
	v_exp_f32_e32 v32, v32
	v_exp_f32_e32 v33, v33
	v_exp_f32_e32 v29, v29
	v_mul_f32_e32 v34, 0xbfb8aa3b, v34
	v_mul_f32_e32 v30, 0xbfb8aa3b, v30
	v_mul_f32_e32 v35, 0xbfb8aa3b, v35
	v_mul_f32_e32 v31, 0xbfb8aa3b, v31
	global_store_dwordx2 v[148:149], v[44:45], off offset:1024 nt
	v_fma_f32 v40, v40, s39, 0.5
	v_cvt_u32_f32_e32 v44, v36
	v_fma_f32 v36, v41, s39, 0.5
	v_fma_f32 v37, v37, s39, 0.5
	v_exp_f32_e32 v34, v34
	v_exp_f32_e32 v30, v30
	v_exp_f32_e32 v35, v35
	v_exp_f32_e32 v31, v31
	v_med3_f32 v40, v40, 1.0, v231
	v_med3_f32 v36, v36, 1.0, v231
	v_med3_f32 v37, v37, 1.0, v231
	v_fma_f32 v41, v42, s39, 0.5
	v_fma_f32 v38, v38, s39, 0.5
	v_fma_f32 v42, v43, s39, 0.5
	v_fma_f32 v39, v39, s39, 0.5
	v_add_f32_e32 v28, 1.0, v28
	v_cvt_u32_f32_e32 v40, v40
	v_cvt_u32_f32_e32 v36, v36
	v_cvt_u32_f32_e32 v37, v37
	v_med3_f32 v41, v41, 1.0, v231
	v_med3_f32 v38, v38, 1.0, v231
	v_med3_f32 v42, v42, 1.0, v231
	v_med3_f32 v39, v39, 1.0, v231
	v_rcp_f32_e32 v28, v28
	v_cvt_u32_f32_sdwa v41, v41 dst_sel:WORD_1 dst_unused:UNUSED_PAD src0_sel:DWORD
	v_cvt_u32_f32_sdwa v38, v38 dst_sel:WORD_1 dst_unused:UNUSED_PAD src0_sel:DWORD
	v_cvt_u32_f32_sdwa v42, v42 dst_sel:BYTE_3 dst_unused:UNUSED_PAD src0_sel:DWORD
	v_cvt_u32_f32_sdwa v39, v39 dst_sel:BYTE_3 dst_unused:UNUSED_PAD src0_sel:DWORD
	v_add_f32_e32 v32, 1.0, v32
	v_add_f32_e32 v33, 1.0, v33
	v_add_f32_e32 v29, 1.0, v29
	v_pk_mul_f32 v[20:21], v[20:21], v[150:151] op_sel_hi:[1,0]
	v_rcp_f32_e32 v32, v32
	v_rcp_f32_e32 v33, v33
	v_rcp_f32_e32 v29, v29
	v_add_f32_e32 v34, 1.0, v34
	v_add_f32_e32 v30, 1.0, v30
	v_add_f32_e32 v35, 1.0, v35
	v_add_f32_e32 v31, 1.0, v31
	v_mul_f32_e32 v20, 0xbfb8aa3b, v20
	v_rcp_f32_e32 v34, v34
	v_rcp_f32_e32 v30, v30
	v_rcp_f32_e32 v35, v35
	v_rcp_f32_e32 v31, v31
	v_pk_mul_f32 v[24:25], v[24:25], v[150:151] op_sel_hi:[1,0]
	v_exp_f32_e32 v20, v20
	v_fmamk_f32 v157, v159, 0x39800000, v221
	s_mov_b64 s[12:13], 0x90000
	v_lshl_or_b32 v36, v36, 8, v40
	v_lshl_or_b32 v37, v37, 8, v44
	v_fma_f32 v28, v28, s39, 0.5
	v_pk_mul_f32 v[26:27], v[26:27], v[150:151] op_sel_hi:[1,0]
	v_mul_f32_e32 v24, 0xbfb8aa3b, v24
	v_pk_mul_f32 v[22:23], v[22:23], v[150:151] op_sel_hi:[1,0]
	v_mul_f32_e32 v25, 0xbfb8aa3b, v25
	v_mul_f32_e32 v21, 0xbfb8aa3b, v21
	v_rsq_f32_e32 v146, v157
	v_lshl_add_u64 v[46:47], v[148:149], 0, s[12:13]
	v_or3_b32 v36, v36, v41, v42
	v_or3_b32 v37, v37, v38, v39
	v_med3_f32 v28, v28, 1.0, v231
	v_exp_f32_e32 v24, v24
	v_exp_f32_e32 v25, v25
	v_exp_f32_e32 v21, v21
	v_mul_f32_e32 v26, 0xbfb8aa3b, v26
	v_mul_f32_e32 v22, 0xbfb8aa3b, v22
	v_mul_f32_e32 v27, 0xbfb8aa3b, v27
	v_mul_f32_e32 v23, 0xbfb8aa3b, v23
	global_store_dwordx2 v[148:149], v[36:37], off offset:1536 nt
	v_fma_f32 v32, v32, s39, 0.5
	v_cvt_u32_f32_e32 v36, v28
	v_fma_f32 v28, v33, s39, 0.5
	v_fma_f32 v29, v29, s39, 0.5
	v_exp_f32_e32 v26, v26
	v_exp_f32_e32 v22, v22
	v_exp_f32_e32 v27, v27
	v_exp_f32_e32 v23, v23
	v_med3_f32 v32, v32, 1.0, v231
	v_med3_f32 v28, v28, 1.0, v231
	v_med3_f32 v29, v29, 1.0, v231
	v_fma_f32 v33, v34, s39, 0.5
	v_fma_f32 v30, v30, s39, 0.5
	v_fma_f32 v34, v35, s39, 0.5
	v_fma_f32 v31, v31, s39, 0.5
	v_add_f32_e32 v20, 1.0, v20
	v_cvt_u32_f32_e32 v32, v32
	v_cvt_u32_f32_e32 v28, v28
	v_cvt_u32_f32_e32 v29, v29
	v_med3_f32 v33, v33, 1.0, v231
	v_med3_f32 v30, v30, 1.0, v231
	v_med3_f32 v34, v34, 1.0, v231
	v_med3_f32 v31, v31, 1.0, v231
	v_rcp_f32_e32 v20, v20
	v_cvt_u32_f32_sdwa v33, v33 dst_sel:WORD_1 dst_unused:UNUSED_PAD src0_sel:DWORD
	v_cvt_u32_f32_sdwa v30, v30 dst_sel:WORD_1 dst_unused:UNUSED_PAD src0_sel:DWORD
	v_cvt_u32_f32_sdwa v34, v34 dst_sel:BYTE_3 dst_unused:UNUSED_PAD src0_sel:DWORD
	v_cvt_u32_f32_sdwa v31, v31 dst_sel:BYTE_3 dst_unused:UNUSED_PAD src0_sel:DWORD
	v_add_f32_e32 v24, 1.0, v24
	v_add_f32_e32 v25, 1.0, v25
	v_add_f32_e32 v21, 1.0, v21
	v_pk_mul_f32 v[12:13], v[12:13], v[146:147] op_sel_hi:[1,0]
	v_rcp_f32_e32 v24, v24
	v_rcp_f32_e32 v25, v25
;     template <int ACT, int AUX> __device__ __forceinline__ void run(const f32x4 (&acc)[2][2][4][2], const Unit& uu, int wr, int wc, int fr, int fq) const {
;     ...
;                 for (int bj = 0; bj < 2; ++bj) { f32x4 v0 = acc[ai][bj][m][0] * rs, v1 = acc[ai][bj][m][1] * rs;
; #pragma unroll
;                     for (int j = 0; j < 4; ++j) { v0[j] = act_f<ACT>(v0[j]); v1[j] = act_f<ACT>(v1[j]); }
;                     if (AUX == 4) {
;                         unsigned q[8];
; #pragma unroll
;                         for (int j = 0; j < 4; ++j) { q[j] = (unsigned)fminf(fmaxf(fmaf(v0[j], 255.0f, 0.5f), 1.0f), 255.0f); q[4 + j] = (unsigned)fminf(fmaxf(fmaf(v1[j], 255.0f, 0.5f), 1.0f), 255.0f); }
;                         u32x2 w8; w8.x = q[0] | (q[1] << 8) | (q[2] << 16) | (q[3] << 24); w8.y = q[4] | (q[5] << 8) | (q[6] << 16) | (q[7] << 24);
;                         __builtin_nontemporal_store(w8, (u32x2*)(g8 + ((size_t)((u.pn - 52) >> 4) * cfg::MT + r) * cfg::DM + ((u.pn - 52) & 15) * BM + wc * 32 + 8 * fq + bj * HALF));
	v_rcp_f32_e32 v21, v21
	v_add_f32_e32 v26, 1.0, v26
	v_add_f32_e32 v22, 1.0, v22
	v_add_f32_e32 v27, 1.0, v27
	v_add_f32_e32 v23, 1.0, v23
	v_mul_f32_e32 v12, 0xbfb8aa3b, v12
	s_mov_b32 s2, 0xa0000
	v_rcp_f32_e32 v26, v26
	v_rcp_f32_e32 v22, v22
	v_rcp_f32_e32 v27, v27
	v_rcp_f32_e32 v23, v23
	v_pk_mul_f32 v[16:17], v[16:17], v[146:147] op_sel_hi:[1,0]
	v_exp_f32_e32 v12, v12
	v_lshl_or_b32 v28, v28, 8, v32
	v_lshl_or_b32 v29, v29, 8, v36
	v_add_co_u32_e32 v32, vcc, s2, v148
	v_fma_f32 v20, v20, s39, 0.5
	v_pk_mul_f32 v[18:19], v[18:19], v[146:147] op_sel_hi:[1,0]
	v_mul_f32_e32 v16, 0xbfb8aa3b, v16
	v_pk_mul_f32 v[14:15], v[14:15], v[146:147] op_sel_hi:[1,0]
	v_mul_f32_e32 v17, 0xbfb8aa3b, v17
	v_mul_f32_e32 v13, 0xbfb8aa3b, v13
	v_or3_b32 v28, v28, v33, v34
	v_or3_b32 v29, v29, v30, v31
	v_addc_co_u32_e32 v33, vcc, 0, v149, vcc
	v_med3_f32 v20, v20, 1.0, v231
	v_exp_f32_e32 v16, v16
	v_exp_f32_e32 v17, v17
	v_exp_f32_e32 v13, v13
	v_mul_f32_e32 v18, 0xbfb8aa3b, v18
	v_mul_f32_e32 v14, 0xbfb8aa3b, v14
	v_mul_f32_e32 v19, 0xbfb8aa3b, v19
	v_mul_f32_e32 v15, 0xbfb8aa3b, v15
	global_store_dwordx2 v[148:149], v[28:29], off offset:2048 nt
	v_fma_f32 v24, v24, s39, 0.5
	v_cvt_u32_f32_e32 v28, v20
	v_fma_f32 v20, v25, s39, 0.5
	v_fma_f32 v21, v21, s39, 0.5
	v_exp_f32_e32 v18, v18
	v_exp_f32_e32 v14, v14
	v_exp_f32_e32 v19, v19
	v_exp_f32_e32 v15, v15
	v_med3_f32 v24, v24, 1.0, v231
	v_med3_f32 v20, v20, 1.0, v231
	v_med3_f32 v21, v21, 1.0, v231
	v_fma_f32 v25, v26, s39, 0.5
	v_fma_f32 v22, v22, s39, 0.5
	v_fma_f32 v26, v27, s39, 0.5
	v_fma_f32 v23, v23, s39, 0.5
	v_add_f32_e32 v12, 1.0, v12
	v_cvt_u32_f32_e32 v24, v24
	v_cvt_u32_f32_e32 v20, v20
	v_cvt_u32_f32_e32 v21, v21
	v_med3_f32 v25, v25, 1.0, v231
	v_med3_f32 v22, v22, 1.0, v231
	v_med3_f32 v26, v26, 1.0, v231
	v_med3_f32 v23, v23, 1.0, v231
	v_rcp_f32_e32 v12, v12
	v_cvt_u32_f32_sdwa v25, v25 dst_sel:WORD_1 dst_unused:UNUSED_PAD src0_sel:DWORD
	v_cvt_u32_f32_sdwa v22, v22 dst_sel:WORD_1 dst_unused:UNUSED_PAD src0_sel:DWORD
	v_cvt_u32_f32_sdwa v26, v26 dst_sel:BYTE_3 dst_unused:UNUSED_PAD src0_sel:DWORD
	v_cvt_u32_f32_sdwa v23, v23 dst_sel:BYTE_3 dst_unused:UNUSED_PAD src0_sel:DWORD
	v_add_f32_e32 v16, 1.0, v16
	v_add_f32_e32 v17, 1.0, v17
	v_add_f32_e32 v13, 1.0, v13
	v_pk_mul_f32 v[4:5], v[4:5], v[146:147] op_sel_hi:[1,0]
	v_rcp_f32_e32 v16, v16
	v_rcp_f32_e32 v17, v17
	v_rcp_f32_e32 v13, v13
	v_add_f32_e32 v18, 1.0, v18
	v_add_f32_e32 v14, 1.0, v14
	v_add_f32_e32 v19, 1.0, v19
	v_add_f32_e32 v15, 1.0, v15
	v_mul_f32_e32 v4, 0xbfb8aa3b, v4
	v_rcp_f32_e32 v18, v18
	v_rcp_f32_e32 v14, v14
	v_rcp_f32_e32 v19, v19
	v_rcp_f32_e32 v15, v15
	v_pk_mul_f32 v[8:9], v[8:9], v[146:147] op_sel_hi:[1,0]
	v_exp_f32_e32 v4, v4
	s_mov_b64 s[12:13], 0xa0000
	v_lshl_or_b32 v20, v20, 8, v24
	v_lshl_or_b32 v21, v21, 8, v28
	v_fma_f32 v12, v12, s39, 0.5
	v_pk_mul_f32 v[10:11], v[10:11], v[146:147] op_sel_hi:[1,0]
	v_mul_f32_e32 v8, 0xbfb8aa3b, v8
	v_pk_mul_f32 v[6:7], v[6:7], v[146:147] op_sel_hi:[1,0]
	v_mul_f32_e32 v9, 0xbfb8aa3b, v9
	v_mul_f32_e32 v5, 0xbfb8aa3b, v5
	v_lshl_add_u64 v[30:31], v[148:149], 0, s[12:13]
	v_or3_b32 v20, v20, v25, v26
	v_or3_b32 v21, v21, v22, v23
	v_med3_f32 v12, v12, 1.0, v231
	v_exp_f32_e32 v8, v8
	v_exp_f32_e32 v9, v9
	v_exp_f32_e32 v5, v5
	v_mul_f32_e32 v10, 0xbfb8aa3b, v10
	v_mul_f32_e32 v6, 0xbfb8aa3b, v6
	v_mul_f32_e32 v11, 0xbfb8aa3b, v11
	v_mul_f32_e32 v7, 0xbfb8aa3b, v7
	global_store_dwordx2 v[148:149], v[20:21], off offset:2560 nt
	v_fma_f32 v16, v16, s39, 0.5
	v_cvt_u32_f32_e32 v20, v12
	v_fma_f32 v12, v17, s39, 0.5
	v_fma_f32 v13, v13, s39, 0.5
	v_exp_f32_e32 v10, v10
	v_exp_f32_e32 v6, v6
	v_exp_f32_e32 v11, v11
	v_exp_f32_e32 v7, v7
	v_med3_f32 v16, v16, 1.0, v231
	v_med3_f32 v12, v12, 1.0, v231
	v_med3_f32 v13, v13, 1.0, v231
	v_fma_f32 v17, v18, s39, 0.5
	v_fma_f32 v14, v14, s39, 0.5
	v_fma_f32 v18, v19, s39, 0.5
	v_fma_f32 v15, v15, s39, 0.5
	v_add_f32_e32 v4, 1.0, v4
	v_cvt_u32_f32_e32 v16, v16
	v_cvt_u32_f32_e32 v12, v12
	v_cvt_u32_f32_e32 v13, v13
	v_med3_f32 v17, v17, 1.0, v231
	v_med3_f32 v14, v14, 1.0, v231
	v_med3_f32 v18, v18, 1.0, v231
	v_med3_f32 v15, v15, 1.0, v231
	v_rcp_f32_e32 v4, v4
	v_cvt_u32_f32_sdwa v17, v17 dst_sel:WORD_1 dst_unused:UNUSED_PAD src0_sel:DWORD
	v_cvt_u32_f32_sdwa v14, v14 dst_sel:WORD_1 dst_unused:UNUSED_PAD src0_sel:DWORD
	v_cvt_u32_f32_sdwa v18, v18 dst_sel:BYTE_3 dst_unused:UNUSED_PAD src0_sel:DWORD
	v_cvt_u32_f32_sdwa v15, v15 dst_sel:BYTE_3 dst_unused:UNUSED_PAD src0_sel:DWORD
	v_add_f32_e32 v8, 1.0, v8
	v_add_f32_e32 v9, 1.0, v9
	v_add_f32_e32 v5, 1.0, v5
	v_rcp_f32_e32 v8, v8
	v_rcp_f32_e32 v9, v9
	v_rcp_f32_e32 v5, v5
	v_add_f32_e32 v10, 1.0, v10
	v_add_f32_e32 v6, 1.0, v6
	v_add_f32_e32 v11, 1.0, v11
	v_add_f32_e32 v7, 1.0, v7
	s_mov_b32 s2, 0xb0000
	v_rcp_f32_e32 v10, v10
	v_rcp_f32_e32 v6, v6
	v_rcp_f32_e32 v11, v11
	v_rcp_f32_e32 v7, v7
	v_lshl_or_b32 v12, v12, 8, v16
	v_lshl_or_b32 v13, v13, 8, v20
	v_add_co_u32_e32 v16, vcc, s2, v148
	v_fma_f32 v4, v4, s39, 0.5
	v_or3_b32 v12, v12, v17, v18
	v_or3_b32 v13, v13, v14, v15
	v_addc_co_u32_e32 v17, vcc, 0, v149, vcc
	v_med3_f32 v4, v4, 1.0, v231
	global_store_dwordx2 v[148:149], v[12:13], off offset:3072 nt
	v_fma_f32 v8, v8, s39, 0.5
	v_cvt_u32_f32_e32 v12, v4
	v_fma_f32 v4, v9, s39, 0.5
	v_fma_f32 v5, v5, s39, 0.5
	v_med3_f32 v8, v8, 1.0, v231
	v_med3_f32 v4, v4, 1.0, v231
	v_med3_f32 v5, v5, 1.0, v231
	v_fma_f32 v9, v10, s39, 0.5
	v_fma_f32 v6, v6, s39, 0.5
	v_fma_f32 v10, v11, s39, 0.5
	v_fma_f32 v7, v7, s39, 0.5
	v_cvt_u32_f32_e32 v8, v8
	v_cvt_u32_f32_e32 v4, v4
	v_cvt_u32_f32_e32 v5, v5
	v_med3_f32 v9, v9, 1.0, v231
	v_med3_f32 v6, v6, 1.0, v231
	v_med3_f32 v10, v10, 1.0, v231
	v_med3_f32 v7, v7, 1.0, v231
	v_cvt_u32_f32_sdwa v9, v9 dst_sel:WORD_1 dst_unused:UNUSED_PAD src0_sel:DWORD
	v_cvt_u32_f32_sdwa v6, v6 dst_sel:WORD_1 dst_unused:UNUSED_PAD src0_sel:DWORD
	v_cvt_u32_f32_sdwa v10, v10 dst_sel:BYTE_3 dst_unused:UNUSED_PAD src0_sel:DWORD
	v_cvt_u32_f32_sdwa v7, v7 dst_sel:BYTE_3 dst_unused:UNUSED_PAD src0_sel:DWORD
	s_mov_b64 s[12:13], 0xb0000
	v_lshl_or_b32 v4, v4, 8, v8
	v_lshl_or_b32 v5, v5, 8, v12
	v_lshl_add_u64 v[14:15], v[148:149], 0, s[12:13]
	v_or3_b32 v4, v4, v9, v10
	v_or3_b32 v5, v5, v6, v7
	global_store_dwordx2 v[148:149], v[4:5], off offset:3584 nt

;     static __device__ __forceinline__ float ub(unsigned w, int k) { return (float)((w >> (8 * k)) & 0xffu); }
;     __device__ __forceinline__ void mid(f32x4 (&acc)[2][2][4][2], const Unit& u, int b, int wr, int wc, int fr, int fq) const {
;         const unsigned char* pa = g8 + ((size_t)(b - 1) * cfg::MT + u.pm * BM + wr * 64 + fr) * cfg::DM + u.pn * BM + wc * 32 + 8 * fq; const unsigned char* pb = pa + (size_t)cfg::MT * cfg::DM;
;         u32x2 ga[16], gb[16];
; #pragma unroll
;         for (int i = 0; i < 16; ++i) { const size_t o = (size_t)(((i >> 3) & 1) * HALF + ((i >> 1) & 3) * 16) * cfg::DM + (i & 1) * HALF;
;             ga[i] = *(const u32x2*)(pa + o); gb[i] = *(const u32x2*)(pb + o); }
;         asm volatile("" ::: "memory");
; #pragma unroll
;         for (int i = 0; i < 16; ++i) { const int ai = (i >> 3) & 1, m = (i >> 1) & 3, bj = i & 1;
;             f32x4 r0, r1;
; #pragma unroll
;             for (int j = 0; j < 4; ++j) { r0[j] = ub(ga[i].x, j) * __builtin_amdgcn_rcpf(ub(gb[i].x, j)); r1[j] = ub(ga[i].y, j) * __builtin_amdgcn_rcpf(ub(gb[i].y, j)); }
;             acc[ai][bj][m][0] *= r0; acc[ai][bj][m][1] *= r1; }
.LBB0_1602:
	s_cmp_eq_u32 s28, 0
	s_cselect_b64 s[12:13], -1, 0
	s_and_b32 s2, s48, 14
	s_cmp_lg_u32 s2, 0
	s_cselect_b64 s[30:31], -1, 0
	s_or_b64 s[12:13], s[12:13], s[30:31]
	s_and_b64 vcc, exec, s[12:13]
	s_cbranch_vccnz .LBB0_1604
	s_and_b64 vcc, exec, s[10:11]
	s_cbranch_vccz .Lp3_hook_lead_done
	s_barrier
.Lp3_hook_lead_done:
	s_lshr_b32 s2, s48, 4
	s_lshl_b64 s[12:13], s[2:3], 25
	s_add_u32 s12, s6, s12
	s_addc_u32 s13, s7, s13
	s_lshl_b32 s2, s24, 12
	s_lshl_b32 s30, s26, 8
	s_add_i32 s2, s2, s30
	s_lshl_b32 s30, s39, 3
	s_add_i32 s2, s2, s30
	s_addk_i32 s2, 0x1000
	s_add_u32 s12, s12, s2
	s_addc_u32 s13, s13, 0
	v_mbcnt_lo_u32_b32 v4, -1, 0
	v_mbcnt_hi_u32_b32 v4, -1, v4
	v_lshlrev_b32_e32 v4, 3, v4
	v_mov_b32_e32 v5, 0
	v_lshl_add_u64 v[222:223], s[12:13], 0, v[4:5]
	s_add_u32 s12, s12, 0xfe000000
	s_addc_u32 s13, s13, -1
	v_lshl_add_u64 v[4:5], s[12:13], 0, v[4:5]
	global_load_dwordx2 v[192:193], v[4:5], off offset:-4096
	global_load_dwordx2 v[194:195], v[222:223], off offset:-4096
	global_load_dwordx2 v[214:215], v[4:5], off offset:-3584
	global_load_dwordx2 v[216:217], v[222:223], off offset:-3584
	global_load_dwordx2 v[210:211], v[4:5], off offset:-3072
	global_load_dwordx2 v[212:213], v[222:223], off offset:-3072
	global_load_dwordx2 v[206:207], v[4:5], off offset:-2560
	global_load_dwordx2 v[208:209], v[222:223], off offset:-2560
	global_load_dwordx2 v[202:203], v[4:5], off offset:-2048
	global_load_dwordx2 v[204:205], v[222:223], off offset:-2048
	global_load_dwordx2 v[198:199], v[4:5], off offset:-1536
	global_load_dwordx2 v[200:201], v[222:223], off offset:-1536
	global_load_dwordx2 v[190:191], v[4:5], off offset:-1024
	global_load_dwordx2 v[196:197], v[222:223], off offset:-1024
	global_load_dwordx2 v[186:187], v[4:5], off offset:-512
	global_load_dwordx2 v[188:189], v[222:223], off offset:-512
	global_load_dwordx2 v[182:183], v[4:5], off
	global_load_dwordx2 v[184:185], v[222:223], off
	global_load_dwordx2 v[178:179], v[4:5], off offset:512
	global_load_dwordx2 v[180:181], v[222:223], off offset:512
	global_load_dwordx2 v[174:175], v[4:5], off offset:1024
	global_load_dwordx2 v[176:177], v[222:223], off offset:1024
	global_load_dwordx2 v[170:171], v[4:5], off offset:1536
	global_load_dwordx2 v[172:173], v[222:223], off offset:1536
	global_load_dwordx2 v[166:167], v[4:5], off offset:2048
	global_load_dwordx2 v[168:169], v[222:223], off offset:2048
	global_load_dwordx2 v[162:163], v[4:5], off offset:2560
	global_load_dwordx2 v[164:165], v[222:223], off offset:2560
	global_load_dwordx2 v[158:159], v[4:5], off offset:3072
	global_load_dwordx2 v[160:161], v[222:223], off offset:3072
	global_load_dwordx2 v[156:157], v[222:223], off offset:3584
	global_load_dwordx2 v[4:5], v[4:5], off offset:3584
	s_waitcnt vmcnt(28)
	v_cvt_f32_ubyte3_e32 v239, v192
	v_cvt_f32_ubyte0_e32 v2, v194
	v_cvt_f32_ubyte2_e32 v238, v192
	v_cvt_f32_ubyte1_e32 v245, v192
	v_cvt_f32_ubyte0_e32 v244, v192
	v_rcp_iflag_f32_e32 v222, v2
	v_cvt_f32_ubyte0_e32 v2, v195
	v_rcp_iflag_f32_e32 v232, v2
	v_cvt_f32_ubyte1_e32 v2, v194
	v_rcp_iflag_f32_e32 v223, v2
	v_cvt_f32_ubyte1_e32 v2, v195
	v_rcp_iflag_f32_e32 v233, v2
	v_cvt_f32_ubyte2_e32 v2, v194
	v_rcp_iflag_f32_e32 v234, v2
	v_cvt_f32_ubyte2_e32 v2, v195
	v_rcp_iflag_f32_e32 v236, v2
	v_cvt_f32_ubyte3_e32 v2, v194
	v_rcp_iflag_f32_e32 v235, v2
	v_cvt_f32_ubyte3_e32 v2, v195
	v_rcp_iflag_f32_e32 v237, v2
	v_cvt_f32_ubyte3_e32 v195, v193
	v_pk_mul_f32 v[234:235], v[234:235], v[238:239]
	v_cvt_f32_ubyte1_e32 v239, v193
	v_cvt_f32_ubyte0_e32 v238, v193
	v_cvt_f32_ubyte2_e32 v194, v193
	v_pk_mul_f32 v[192:193], v[232:233], v[238:239]
	v_cvt_f32_ubyte0_e32 v2, v216
	v_pk_mul_f32 v[194:195], v[236:237], v[194:195]
	v_pk_mul_f32 v[126:127], v[126:127], v[192:193]
	v_rcp_iflag_f32_e32 v192, v2
	v_cvt_f32_ubyte0_e32 v2, v217
	v_pk_mul_f32 v[128:129], v[128:129], v[194:195]
	v_rcp_iflag_f32_e32 v194, v2
	v_cvt_f32_ubyte1_e32 v2, v216
	v_rcp_iflag_f32_e32 v193, v2
	v_cvt_f32_ubyte1_e32 v2, v217
	v_pk_mul_f32 v[222:223], v[222:223], v[244:245]
	v_rcp_iflag_f32_e32 v195, v2
	v_cvt_f32_ubyte2_e32 v2, v216
	v_pk_mul_f32 v[130:131], v[130:131], v[222:223]
	v_rcp_iflag_f32_e32 v222, v2
	v_cvt_f32_ubyte2_e32 v2, v217
	v_rcp_iflag_f32_e32 v232, v2
	v_cvt_f32_ubyte3_e32 v2, v216
	v_rcp_iflag_f32_e32 v223, v2
	v_pk_mul_f32 v[132:133], v[132:133], v[234:235]
	v_cvt_f32_ubyte3_e32 v235, v214
	v_cvt_f32_ubyte2_e32 v234, v214
	v_cvt_f32_ubyte1_e32 v237, v214
	v_cvt_f32_ubyte0_e32 v236, v214
	v_cvt_f32_ubyte3_e32 v2, v217
	v_pk_mul_f32 v[192:193], v[192:193], v[236:237]
	v_pk_mul_f32 v[222:223], v[222:223], v[234:235]
	v_rcp_iflag_f32_e32 v233, v2
	v_cvt_f32_ubyte1_e32 v235, v215
	v_cvt_f32_ubyte0_e32 v234, v215
	s_waitcnt vmcnt(0)
;     static __device__ __forceinline__ float ub(unsigned w, int k) { return (float)((w >> (8 * k)) & 0xffu); }
;     __device__ __forceinline__ void mid(f32x4 (&acc)[2][2][4][2], const Unit& u, int b, int wr, int wc, int fr, int fq) const {
;     ...
;         for (int i = 0; i < 16; ++i) { const int ai = (i >> 3) & 1, m = (i >> 1) & 3, bj = i & 1;
;             f32x4 r0, r1;
; #pragma unroll
;             for (int j = 0; j < 4; ++j) { r0[j] = ub(ga[i].x, j) * __builtin_amdgcn_rcpf(ub(gb[i].x, j)); r1[j] = ub(ga[i].y, j) * __builtin_amdgcn_rcpf(ub(gb[i].y, j)); }
;             acc[ai][bj][m][0] *= r0; acc[ai][bj][m][1] *= r1; }
	v_cvt_f32_ubyte0_e32 v2, v212
	v_pk_mul_f32 v[194:195], v[194:195], v[234:235]
	v_pk_mul_f32 v[122:123], v[122:123], v[192:193]
	v_rcp_iflag_f32_e32 v192, v2
	v_cvt_f32_ubyte0_e32 v2, v213
	v_pk_mul_f32 v[118:119], v[118:119], v[194:195]
	v_rcp_iflag_f32_e32 v194, v2
	v_cvt_f32_ubyte1_e32 v2, v212
	v_cvt_f32_ubyte3_e32 v217, v215
	v_cvt_f32_ubyte2_e32 v216, v215
	v_rcp_iflag_f32_e32 v193, v2
	v_cvt_f32_ubyte1_e32 v2, v213
	v_pk_mul_f32 v[214:215], v[232:233], v[216:217]
	v_rcp_iflag_f32_e32 v195, v2
	v_cvt_f32_ubyte2_e32 v2, v212
	v_pk_mul_f32 v[120:121], v[120:121], v[214:215]
	v_rcp_iflag_f32_e32 v214, v2
	v_cvt_f32_ubyte2_e32 v2, v213
	v_rcp_iflag_f32_e32 v216, v2
	v_cvt_f32_ubyte3_e32 v2, v212
	v_rcp_iflag_f32_e32 v215, v2
	v_pk_mul_f32 v[124:125], v[124:125], v[222:223]
	v_cvt_f32_ubyte3_e32 v223, v210
	v_cvt_f32_ubyte2_e32 v222, v210
	v_cvt_f32_ubyte1_e32 v233, v210
	v_cvt_f32_ubyte0_e32 v232, v210
	v_cvt_f32_ubyte3_e32 v2, v213
	v_pk_mul_f32 v[192:193], v[192:193], v[232:233]
	v_pk_mul_f32 v[214:215], v[214:215], v[222:223]
	v_rcp_iflag_f32_e32 v217, v2
	v_cvt_f32_ubyte1_e32 v223, v211
	v_cvt_f32_ubyte0_e32 v222, v211
	v_cvt_f32_ubyte0_e32 v2, v208
	v_pk_mul_f32 v[194:195], v[194:195], v[222:223]
	v_pk_mul_f32 v[114:115], v[114:115], v[192:193]
	v_rcp_iflag_f32_e32 v192, v2
	v_cvt_f32_ubyte0_e32 v2, v209
	v_pk_mul_f32 v[110:111], v[110:111], v[194:195]
	v_rcp_iflag_f32_e32 v194, v2
	v_cvt_f32_ubyte1_e32 v2, v208
	v_cvt_f32_ubyte3_e32 v213, v211
	v_cvt_f32_ubyte2_e32 v212, v211
	v_rcp_iflag_f32_e32 v193, v2
	v_cvt_f32_ubyte1_e32 v2, v209
	v_pk_mul_f32 v[210:211], v[216:217], v[212:213]
	v_rcp_iflag_f32_e32 v195, v2
	v_cvt_f32_ubyte2_e32 v2, v208
	v_pk_mul_f32 v[112:113], v[112:113], v[210:211]
	v_rcp_iflag_f32_e32 v210, v2
	v_cvt_f32_ubyte2_e32 v2, v209
	v_rcp_iflag_f32_e32 v212, v2
	v_cvt_f32_ubyte3_e32 v2, v208
	v_rcp_iflag_f32_e32 v211, v2
	v_pk_mul_f32 v[116:117], v[116:117], v[214:215]
	v_cvt_f32_ubyte3_e32 v215, v206
	v_cvt_f32_ubyte2_e32 v214, v206
	v_cvt_f32_ubyte1_e32 v217, v206
	v_cvt_f32_ubyte0_e32 v216, v206
	v_cvt_f32_ubyte3_e32 v2, v209
	v_pk_mul_f32 v[192:193], v[192:193], v[216:217]
	v_pk_mul_f32 v[210:211], v[210:211], v[214:215]
	v_rcp_iflag_f32_e32 v213, v2
	v_cvt_f32_ubyte1_e32 v215, v207
	v_cvt_f32_ubyte0_e32 v214, v207
	v_cvt_f32_ubyte0_e32 v2, v204
	v_pk_mul_f32 v[194:195], v[194:195], v[214:215]
	v_pk_mul_f32 v[106:107], v[106:107], v[192:193]
	v_rcp_iflag_f32_e32 v192, v2
	v_cvt_f32_ubyte0_e32 v2, v205
	v_pk_mul_f32 v[102:103], v[102:103], v[194:195]
	v_rcp_iflag_f32_e32 v194, v2
	v_cvt_f32_ubyte1_e32 v2, v204
	v_cvt_f32_ubyte3_e32 v209, v207
	v_cvt_f32_ubyte2_e32 v208, v207
	v_rcp_iflag_f32_e32 v193, v2
	v_cvt_f32_ubyte1_e32 v2, v205
	v_pk_mul_f32 v[206:207], v[212:213], v[208:209]
	v_rcp_iflag_f32_e32 v195, v2
	v_cvt_f32_ubyte2_e32 v2, v204
	v_pk_mul_f32 v[104:105], v[104:105], v[206:207]
	v_rcp_iflag_f32_e32 v206, v2
	v_cvt_f32_ubyte2_e32 v2, v205
	v_rcp_iflag_f32_e32 v208, v2
	v_cvt_f32_ubyte3_e32 v2, v204
	v_rcp_iflag_f32_e32 v207, v2
	v_pk_mul_f32 v[108:109], v[108:109], v[210:211]
	v_cvt_f32_ubyte3_e32 v211, v202
	v_cvt_f32_ubyte2_e32 v210, v202
	v_cvt_f32_ubyte1_e32 v213, v202
	v_cvt_f32_ubyte0_e32 v212, v202
	v_cvt_f32_ubyte3_e32 v2, v205
	v_pk_mul_f32 v[192:193], v[192:193], v[212:213]
	v_pk_mul_f32 v[206:207], v[206:207], v[210:211]
	v_rcp_iflag_f32_e32 v209, v2
	v_cvt_f32_ubyte1_e32 v211, v203
	v_cvt_f32_ubyte0_e32 v210, v203
	v_cvt_f32_ubyte0_e32 v2, v200
	v_pk_mul_f32 v[194:195], v[194:195], v[210:211]
	v_pk_mul_f32 v[98:99], v[98:99], v[192:193]
	v_rcp_iflag_f32_e32 v192, v2
	v_cvt_f32_ubyte0_e32 v2, v201
	v_pk_mul_f32 v[94:95], v[94:95], v[194:195]
	v_rcp_iflag_f32_e32 v194, v2
	v_cvt_f32_ubyte1_e32 v2, v200
	v_cvt_f32_ubyte3_e32 v205, v203
	v_cvt_f32_ubyte2_e32 v204, v203
	v_rcp_iflag_f32_e32 v193, v2
	v_cvt_f32_ubyte1_e32 v2, v201
	v_pk_mul_f32 v[202:203], v[208:209], v[204:205]
	v_rcp_iflag_f32_e32 v195, v2
	v_cvt_f32_ubyte2_e32 v2, v200
	v_pk_mul_f32 v[96:97], v[96:97], v[202:203]
	v_rcp_iflag_f32_e32 v202, v2
	v_cvt_f32_ubyte2_e32 v2, v201
	v_rcp_iflag_f32_e32 v204, v2
	v_cvt_f32_ubyte3_e32 v2, v200
	v_rcp_iflag_f32_e32 v203, v2
	v_pk_mul_f32 v[100:101], v[100:101], v[206:207]
	v_cvt_f32_ubyte3_e32 v207, v198
	v_cvt_f32_ubyte2_e32 v206, v198
	v_cvt_f32_ubyte1_e32 v209, v198
	v_cvt_f32_ubyte0_e32 v208, v198
	v_cvt_f32_ubyte3_e32 v2, v201
	v_pk_mul_f32 v[192:193], v[192:193], v[208:209]
	v_pk_mul_f32 v[202:203], v[202:203], v[206:207]
	v_rcp_iflag_f32_e32 v205, v2
	v_cvt_f32_ubyte1_e32 v207, v199
	v_cvt_f32_ubyte0_e32 v206, v199
	v_cvt_f32_ubyte0_e32 v2, v196
	v_pk_mul_f32 v[194:195], v[194:195], v[206:207]
	v_pk_mul_f32 v[90:91], v[90:91], v[192:193]
	v_rcp_iflag_f32_e32 v192, v2
	v_cvt_f32_ubyte0_e32 v2, v197
	v_pk_mul_f32 v[86:87], v[86:87], v[194:195]
	v_rcp_iflag_f32_e32 v194, v2
	v_cvt_f32_ubyte1_e32 v2, v196
	v_cvt_f32_ubyte3_e32 v201, v199
	v_cvt_f32_ubyte2_e32 v200, v199
	v_rcp_iflag_f32_e32 v193, v2
	v_cvt_f32_ubyte1_e32 v2, v197
	v_pk_mul_f32 v[198:199], v[204:205], v[200:201]
	v_rcp_iflag_f32_e32 v195, v2
	v_cvt_f32_ubyte2_e32 v2, v196
	v_pk_mul_f32 v[88:89], v[88:89], v[198:199]
	v_rcp_iflag_f32_e32 v198, v2
	v_cvt_f32_ubyte2_e32 v2, v197
	v_rcp_iflag_f32_e32 v200, v2
	v_cvt_f32_ubyte3_e32 v2, v196
	v_rcp_iflag_f32_e32 v199, v2
	v_pk_mul_f32 v[92:93], v[92:93], v[202:203]
	v_cvt_f32_ubyte3_e32 v203, v190
	v_cvt_f32_ubyte2_e32 v202, v190
	v_pk_mul_f32 v[198:199], v[198:199], v[202:203]
	v_cvt_f32_ubyte3_e32 v2, v197
	v_cvt_f32_ubyte1_e32 v203, v191
	v_cvt_f32_ubyte0_e32 v202, v191
	v_cvt_f32_ubyte1_e32 v205, v190
	v_cvt_f32_ubyte0_e32 v204, v190
	v_rcp_iflag_f32_e32 v201, v2
;     static __device__ __forceinline__ float ub(unsigned w, int k) { return (float)((w >> (8 * k)) & 0xffu); }
;     __device__ __forceinline__ void mid(f32x4 (&acc)[2][2][4][2], const Unit& u, int b, int wr, int wc, int fr, int fq) const {
;     ...
;         for (int i = 0; i < 16; ++i) { const int ai = (i >> 3) & 1, m = (i >> 1) & 3, bj = i & 1;
;             f32x4 r0, r1;
; #pragma unroll
;             for (int j = 0; j < 4; ++j) { r0[j] = ub(ga[i].x, j) * __builtin_amdgcn_rcpf(ub(gb[i].x, j)); r1[j] = ub(ga[i].y, j) * __builtin_amdgcn_rcpf(ub(gb[i].y, j)); }
;             acc[ai][bj][m][0] *= r0; acc[ai][bj][m][1] *= r1; }
	v_cvt_f32_ubyte3_e32 v197, v191
	v_cvt_f32_ubyte2_e32 v196, v191
	v_pk_mul_f32 v[190:191], v[194:195], v[202:203]
	v_cvt_f32_ubyte0_e32 v2, v188
	v_pk_mul_f32 v[192:193], v[192:193], v[204:205]
	v_pk_mul_f32 v[78:79], v[78:79], v[190:191]
	v_rcp_iflag_f32_e32 v190, v2
	v_cvt_f32_ubyte0_e32 v2, v189
	v_pk_mul_f32 v[82:83], v[82:83], v[192:193]
	v_rcp_iflag_f32_e32 v192, v2
	v_cvt_f32_ubyte1_e32 v2, v188
	v_rcp_iflag_f32_e32 v191, v2
	v_cvt_f32_ubyte1_e32 v2, v189
	v_pk_mul_f32 v[194:195], v[200:201], v[196:197]
	v_rcp_iflag_f32_e32 v193, v2
	v_cvt_f32_ubyte2_e32 v2, v188
	v_pk_mul_f32 v[80:81], v[80:81], v[194:195]
	v_rcp_iflag_f32_e32 v194, v2
	v_cvt_f32_ubyte2_e32 v2, v189
	v_rcp_iflag_f32_e32 v196, v2
	v_cvt_f32_ubyte3_e32 v2, v188
	v_rcp_iflag_f32_e32 v195, v2
	v_cvt_f32_ubyte3_e32 v2, v189
	v_rcp_iflag_f32_e32 v197, v2
	v_pk_mul_f32 v[84:85], v[84:85], v[198:199]
	v_cvt_f32_ubyte3_e32 v199, v186
	v_cvt_f32_ubyte2_e32 v198, v186
	v_pk_mul_f32 v[194:195], v[194:195], v[198:199]
	v_cvt_f32_ubyte1_e32 v199, v187
	v_cvt_f32_ubyte0_e32 v198, v187
	v_cvt_f32_ubyte1_e32 v201, v186
	v_cvt_f32_ubyte0_e32 v200, v186
	v_cvt_f32_ubyte3_e32 v189, v187
	v_cvt_f32_ubyte2_e32 v188, v187
	v_pk_mul_f32 v[186:187], v[192:193], v[198:199]
	v_cvt_f32_ubyte0_e32 v2, v184
	v_pk_mul_f32 v[188:189], v[196:197], v[188:189]
	v_pk_mul_f32 v[70:71], v[70:71], v[186:187]
	v_rcp_iflag_f32_e32 v186, v2
	v_cvt_f32_ubyte0_e32 v2, v185
	v_pk_mul_f32 v[72:73], v[72:73], v[188:189]
	v_rcp_iflag_f32_e32 v188, v2
	v_cvt_f32_ubyte1_e32 v2, v184
	v_rcp_iflag_f32_e32 v187, v2
	v_cvt_f32_ubyte1_e32 v2, v185
	v_pk_mul_f32 v[190:191], v[190:191], v[200:201]
	v_rcp_iflag_f32_e32 v189, v2
	v_cvt_f32_ubyte2_e32 v2, v184
	v_pk_mul_f32 v[74:75], v[74:75], v[190:191]
	v_rcp_iflag_f32_e32 v190, v2
	v_cvt_f32_ubyte2_e32 v2, v185
	v_rcp_iflag_f32_e32 v192, v2
	v_cvt_f32_ubyte3_e32 v2, v184
	v_rcp_iflag_f32_e32 v191, v2
	v_cvt_f32_ubyte3_e32 v2, v185
	v_rcp_iflag_f32_e32 v193, v2
	v_pk_mul_f32 v[76:77], v[76:77], v[194:195]
	v_cvt_f32_ubyte3_e32 v195, v182
	v_cvt_f32_ubyte2_e32 v194, v182
	v_pk_mul_f32 v[190:191], v[190:191], v[194:195]
	v_cvt_f32_ubyte1_e32 v195, v183
	v_cvt_f32_ubyte0_e32 v194, v183
	v_cvt_f32_ubyte1_e32 v197, v182
	v_cvt_f32_ubyte0_e32 v196, v182
	v_cvt_f32_ubyte3_e32 v185, v183
	v_cvt_f32_ubyte2_e32 v184, v183
	v_pk_mul_f32 v[182:183], v[188:189], v[194:195]
	v_cvt_f32_ubyte0_e32 v2, v180
	v_pk_mul_f32 v[184:185], v[192:193], v[184:185]
	v_pk_mul_f32 v[62:63], v[62:63], v[182:183]
	v_rcp_iflag_f32_e32 v182, v2
	v_cvt_f32_ubyte0_e32 v2, v181
	v_pk_mul_f32 v[64:65], v[64:65], v[184:185]
	v_rcp_iflag_f32_e32 v184, v2
	v_cvt_f32_ubyte1_e32 v2, v180
	v_rcp_iflag_f32_e32 v183, v2
	v_cvt_f32_ubyte1_e32 v2, v181
	v_pk_mul_f32 v[186:187], v[186:187], v[196:197]
	v_rcp_iflag_f32_e32 v185, v2
	v_cvt_f32_ubyte2_e32 v2, v180
	v_pk_mul_f32 v[66:67], v[66:67], v[186:187]
	v_rcp_iflag_f32_e32 v186, v2
	v_cvt_f32_ubyte2_e32 v2, v181
	v_rcp_iflag_f32_e32 v188, v2
	v_cvt_f32_ubyte3_e32 v2, v180
	v_rcp_iflag_f32_e32 v187, v2
	v_cvt_f32_ubyte3_e32 v2, v181
	v_rcp_iflag_f32_e32 v189, v2
	v_pk_mul_f32 v[68:69], v[68:69], v[190:191]
	v_cvt_f32_ubyte3_e32 v191, v178
	v_cvt_f32_ubyte2_e32 v190, v178
	v_pk_mul_f32 v[186:187], v[186:187], v[190:191]
	v_cvt_f32_ubyte1_e32 v191, v179
	v_cvt_f32_ubyte0_e32 v190, v179
	v_cvt_f32_ubyte1_e32 v193, v178
	v_cvt_f32_ubyte0_e32 v192, v178
	v_cvt_f32_ubyte3_e32 v181, v179
	v_cvt_f32_ubyte2_e32 v180, v179
	v_pk_mul_f32 v[178:179], v[184:185], v[190:191]
	v_cvt_f32_ubyte0_e32 v2, v176
	v_pk_mul_f32 v[180:181], v[188:189], v[180:181]
	v_pk_mul_f32 v[54:55], v[54:55], v[178:179]
	v_rcp_iflag_f32_e32 v178, v2
	v_cvt_f32_ubyte0_e32 v2, v177
	v_pk_mul_f32 v[56:57], v[56:57], v[180:181]
	v_rcp_iflag_f32_e32 v180, v2
	v_cvt_f32_ubyte1_e32 v2, v176
	v_rcp_iflag_f32_e32 v179, v2
	v_cvt_f32_ubyte1_e32 v2, v177
	v_pk_mul_f32 v[182:183], v[182:183], v[192:193]
	v_rcp_iflag_f32_e32 v181, v2
	v_cvt_f32_ubyte2_e32 v2, v176
	v_pk_mul_f32 v[58:59], v[58:59], v[182:183]
	v_rcp_iflag_f32_e32 v182, v2
	v_cvt_f32_ubyte2_e32 v2, v177
	v_rcp_iflag_f32_e32 v184, v2
	v_cvt_f32_ubyte3_e32 v2, v176
	v_rcp_iflag_f32_e32 v183, v2
	v_cvt_f32_ubyte3_e32 v2, v177
	v_rcp_iflag_f32_e32 v185, v2
	v_pk_mul_f32 v[60:61], v[60:61], v[186:187]
	v_cvt_f32_ubyte3_e32 v187, v174
	v_cvt_f32_ubyte2_e32 v186, v174
	v_pk_mul_f32 v[182:183], v[182:183], v[186:187]
	v_cvt_f32_ubyte1_e32 v187, v175
	v_cvt_f32_ubyte0_e32 v186, v175
	v_cvt_f32_ubyte1_e32 v189, v174
	v_cvt_f32_ubyte0_e32 v188, v174
	v_cvt_f32_ubyte3_e32 v177, v175
	v_cvt_f32_ubyte2_e32 v176, v175
	v_pk_mul_f32 v[174:175], v[180:181], v[186:187]
	v_cvt_f32_ubyte0_e32 v2, v172
	v_pk_mul_f32 v[176:177], v[184:185], v[176:177]
	v_pk_mul_f32 v[46:47], v[46:47], v[174:175]
	v_rcp_iflag_f32_e32 v174, v2
	v_cvt_f32_ubyte0_e32 v2, v173
	v_pk_mul_f32 v[48:49], v[48:49], v[176:177]
	v_rcp_iflag_f32_e32 v176, v2
	v_cvt_f32_ubyte1_e32 v2, v172
	v_rcp_iflag_f32_e32 v175, v2
	v_cvt_f32_ubyte1_e32 v2, v173
	v_pk_mul_f32 v[178:179], v[178:179], v[188:189]
	v_rcp_iflag_f32_e32 v177, v2
	v_cvt_f32_ubyte2_e32 v2, v172
	v_pk_mul_f32 v[50:51], v[50:51], v[178:179]
	v_rcp_iflag_f32_e32 v178, v2
	v_cvt_f32_ubyte2_e32 v2, v173
	v_rcp_iflag_f32_e32 v180, v2
	v_cvt_f32_ubyte3_e32 v2, v172
	v_rcp_iflag_f32_e32 v179, v2
;     static __device__ __forceinline__ float ub(unsigned w, int k) { return (float)((w >> (8 * k)) & 0xffu); }
;     __device__ __forceinline__ void mid(f32x4 (&acc)[2][2][4][2], const Unit& u, int b, int wr, int wc, int fr, int fq) const {
;     ...
;         for (int i = 0; i < 16; ++i) { const int ai = (i >> 3) & 1, m = (i >> 1) & 3, bj = i & 1;
;             f32x4 r0, r1;
; #pragma unroll
;             for (int j = 0; j < 4; ++j) { r0[j] = ub(ga[i].x, j) * __builtin_amdgcn_rcpf(ub(gb[i].x, j)); r1[j] = ub(ga[i].y, j) * __builtin_amdgcn_rcpf(ub(gb[i].y, j)); }
;             acc[ai][bj][m][0] *= r0; acc[ai][bj][m][1] *= r1; }
	v_cvt_f32_ubyte3_e32 v2, v173
	v_rcp_iflag_f32_e32 v181, v2
	v_pk_mul_f32 v[52:53], v[52:53], v[182:183]
	v_cvt_f32_ubyte3_e32 v183, v170
	v_cvt_f32_ubyte2_e32 v182, v170
	v_pk_mul_f32 v[178:179], v[178:179], v[182:183]
	v_cvt_f32_ubyte1_e32 v183, v171
	v_cvt_f32_ubyte0_e32 v182, v171
	v_cvt_f32_ubyte1_e32 v185, v170
	v_cvt_f32_ubyte0_e32 v184, v170
	v_cvt_f32_ubyte3_e32 v173, v171
	v_cvt_f32_ubyte2_e32 v172, v171
	v_pk_mul_f32 v[170:171], v[176:177], v[182:183]
	v_cvt_f32_ubyte0_e32 v2, v168
	v_pk_mul_f32 v[172:173], v[180:181], v[172:173]
	v_pk_mul_f32 v[38:39], v[38:39], v[170:171]
	v_rcp_iflag_f32_e32 v170, v2
	v_cvt_f32_ubyte0_e32 v2, v169
	v_pk_mul_f32 v[40:41], v[40:41], v[172:173]
	v_rcp_iflag_f32_e32 v172, v2
	v_cvt_f32_ubyte1_e32 v2, v168
	v_rcp_iflag_f32_e32 v171, v2
	v_cvt_f32_ubyte1_e32 v2, v169
	v_pk_mul_f32 v[174:175], v[174:175], v[184:185]
	v_rcp_iflag_f32_e32 v173, v2
	v_cvt_f32_ubyte2_e32 v2, v168
	v_pk_mul_f32 v[42:43], v[42:43], v[174:175]
	v_rcp_iflag_f32_e32 v174, v2
	v_cvt_f32_ubyte2_e32 v2, v169
	v_rcp_iflag_f32_e32 v176, v2
	v_cvt_f32_ubyte3_e32 v2, v168
	v_rcp_iflag_f32_e32 v175, v2
	v_cvt_f32_ubyte3_e32 v2, v169
	v_rcp_iflag_f32_e32 v177, v2
	v_pk_mul_f32 v[44:45], v[44:45], v[178:179]
	v_cvt_f32_ubyte3_e32 v179, v166
	v_cvt_f32_ubyte2_e32 v178, v166
	v_pk_mul_f32 v[174:175], v[174:175], v[178:179]
	v_cvt_f32_ubyte1_e32 v179, v167
	v_cvt_f32_ubyte0_e32 v178, v167
	v_cvt_f32_ubyte1_e32 v181, v166
	v_cvt_f32_ubyte0_e32 v180, v166
	v_cvt_f32_ubyte3_e32 v169, v167
	v_cvt_f32_ubyte2_e32 v168, v167
	v_pk_mul_f32 v[166:167], v[172:173], v[178:179]
	v_cvt_f32_ubyte0_e32 v2, v164
	v_pk_mul_f32 v[168:169], v[176:177], v[168:169]
	v_pk_mul_f32 v[30:31], v[30:31], v[166:167]
	v_rcp_iflag_f32_e32 v166, v2
	v_cvt_f32_ubyte0_e32 v2, v165
	v_pk_mul_f32 v[32:33], v[32:33], v[168:169]
	v_rcp_iflag_f32_e32 v168, v2
	v_cvt_f32_ubyte1_e32 v2, v164
	v_rcp_iflag_f32_e32 v167, v2
	v_cvt_f32_ubyte1_e32 v2, v165
	v_pk_mul_f32 v[170:171], v[170:171], v[180:181]
	v_rcp_iflag_f32_e32 v169, v2
	v_cvt_f32_ubyte2_e32 v2, v164
	v_pk_mul_f32 v[34:35], v[34:35], v[170:171]
	v_rcp_iflag_f32_e32 v170, v2
	v_cvt_f32_ubyte2_e32 v2, v165
	v_rcp_iflag_f32_e32 v172, v2
	v_cvt_f32_ubyte3_e32 v2, v164
	v_rcp_iflag_f32_e32 v171, v2
	v_cvt_f32_ubyte3_e32 v2, v165
	v_rcp_iflag_f32_e32 v173, v2
	v_pk_mul_f32 v[36:37], v[36:37], v[174:175]
	v_cvt_f32_ubyte3_e32 v175, v162
	v_cvt_f32_ubyte2_e32 v174, v162
	v_pk_mul_f32 v[170:171], v[170:171], v[174:175]
	v_cvt_f32_ubyte1_e32 v175, v163
	v_cvt_f32_ubyte0_e32 v174, v163
	v_cvt_f32_ubyte1_e32 v177, v162
	v_cvt_f32_ubyte0_e32 v176, v162
	v_cvt_f32_ubyte3_e32 v165, v163
	v_cvt_f32_ubyte2_e32 v164, v163
	v_pk_mul_f32 v[162:163], v[168:169], v[174:175]
	v_cvt_f32_ubyte0_e32 v2, v160
	v_pk_mul_f32 v[164:165], v[172:173], v[164:165]
	v_pk_mul_f32 v[22:23], v[22:23], v[162:163]
	v_rcp_iflag_f32_e32 v162, v2
	v_cvt_f32_ubyte0_e32 v2, v161
	v_pk_mul_f32 v[24:25], v[24:25], v[164:165]
	v_rcp_iflag_f32_e32 v164, v2
	v_cvt_f32_ubyte1_e32 v2, v160
	v_rcp_iflag_f32_e32 v163, v2
	v_cvt_f32_ubyte1_e32 v2, v161
	v_pk_mul_f32 v[166:167], v[166:167], v[176:177]
	v_rcp_iflag_f32_e32 v165, v2
	v_cvt_f32_ubyte2_e32 v2, v160
	v_pk_mul_f32 v[26:27], v[26:27], v[166:167]
	v_rcp_iflag_f32_e32 v166, v2
	v_cvt_f32_ubyte2_e32 v2, v161
	v_rcp_iflag_f32_e32 v168, v2
	v_cvt_f32_ubyte3_e32 v2, v160
	v_rcp_iflag_f32_e32 v167, v2
	v_cvt_f32_ubyte3_e32 v2, v161
	v_rcp_iflag_f32_e32 v169, v2
	v_pk_mul_f32 v[28:29], v[28:29], v[170:171]
	v_cvt_f32_ubyte3_e32 v171, v158
	v_cvt_f32_ubyte2_e32 v170, v158
	v_pk_mul_f32 v[166:167], v[166:167], v[170:171]
	v_cvt_f32_ubyte1_e32 v171, v159
	v_cvt_f32_ubyte0_e32 v170, v159
	v_cvt_f32_ubyte1_e32 v173, v158
	v_cvt_f32_ubyte0_e32 v172, v158
	v_cvt_f32_ubyte3_e32 v161, v159
	v_cvt_f32_ubyte2_e32 v160, v159
	v_pk_mul_f32 v[158:159], v[164:165], v[170:171]
	v_cvt_f32_ubyte0_e32 v2, v156
	v_pk_mul_f32 v[160:161], v[168:169], v[160:161]
	v_pk_mul_f32 v[14:15], v[14:15], v[158:159]
	v_rcp_iflag_f32_e32 v158, v2
	v_cvt_f32_ubyte0_e32 v2, v157
	v_pk_mul_f32 v[16:17], v[16:17], v[160:161]
	v_rcp_iflag_f32_e32 v160, v2
	v_cvt_f32_ubyte1_e32 v2, v156
	v_rcp_iflag_f32_e32 v159, v2
	v_cvt_f32_ubyte1_e32 v2, v157
	v_pk_mul_f32 v[162:163], v[162:163], v[172:173]
	v_rcp_iflag_f32_e32 v161, v2
	v_cvt_f32_ubyte2_e32 v2, v156
	v_pk_mul_f32 v[18:19], v[18:19], v[162:163]
	v_rcp_iflag_f32_e32 v162, v2
	v_cvt_f32_ubyte2_e32 v2, v157
	v_rcp_iflag_f32_e32 v164, v2
	v_cvt_f32_ubyte3_e32 v2, v156
	v_rcp_iflag_f32_e32 v163, v2
	v_cvt_f32_ubyte3_e32 v2, v157
	v_rcp_iflag_f32_e32 v165, v2
	v_pk_mul_f32 v[20:21], v[20:21], v[166:167]
	v_cvt_f32_ubyte3_e32 v167, v4
	v_cvt_f32_ubyte2_e32 v166, v4
	v_cvt_f32_ubyte1_e32 v169, v4
	v_cvt_f32_ubyte0_e32 v168, v4
	v_pk_mul_f32 v[162:163], v[162:163], v[166:167]
	v_cvt_f32_ubyte3_e32 v157, v5
	v_cvt_f32_ubyte2_e32 v156, v5
	v_cvt_f32_ubyte1_e32 v167, v5
	v_cvt_f32_ubyte0_e32 v166, v5
	v_pk_mul_f32 v[158:159], v[158:159], v[168:169]
	v_pk_mul_f32 v[4:5], v[160:161], v[166:167]
	v_pk_mul_f32 v[156:157], v[164:165], v[156:157]
	v_pk_mul_f32 v[12:13], v[12:13], v[162:163]
	v_pk_mul_f32 v[10:11], v[10:11], v[158:159]
	v_pk_mul_f32 v[8:9], v[8:9], v[156:157]
	v_pk_mul_f32 v[6:7], v[6:7], v[4:5]
	s_and_b64 vcc, exec, s[4:5]
	s_cbranch_vccz .LBB0_1604
	s_barrier

; __device__ __forceinline__ unsigned cvt_pk_bf16(float lo, float hi) { f32x2_t v = {lo, hi}; bf16x2_t b = __builtin_convertvector(v, bf16x2_t); return __builtin_bit_cast(unsigned, b); }
;     static __device__ __forceinline__ float ub(unsigned w, int k) { return (float)((w >> (8 * k)) & 0xffu); }
;     __device__ __forceinline__ void operator()(const f32x4 (&acc)[2][2][4][2], const Unit& u, int wr, int wc, int fr, int fq) const {
;         const int row0 = u.pm * BM + wr * 64 + fr, col0 = u.pn * BM + wc * 32 + 8 * fq;
;         const unsigned char* pa = g8 + ((size_t)3 * cfg::MT + row0) * cfg::DM + col0;
;         u32x2 ga[16];
; #pragma unroll
;         for (int i = 0; i < 16; ++i) ga[i] = *(const u32x2*)(pa + (size_t)(((i >> 3) & 1) * HALF + ((i >> 1) & 3) * 16) * cfg::DM + (i & 1) * HALF);
;         asm volatile("" ::: "memory");
; #pragma unroll
;         for (int i = 0; i < 16; ++i) { const int ai = (i >> 3) & 1, m = (i >> 1) & 3, bj = i & 1; const int r = row0 + ai * HALF + m * 16, c = col0 + bj * HALF;
;             f32x4 s0, s1;
; #pragma unroll
;             for (int j = 0; j < 4; ++j) { s0[j] = ub(ga[i].x, j) * (1.0f / 255.0f); s1[j] = ub(ga[i].y, j) * (1.0f / 255.0f); }
;             const f32x4 v0 = acc[ai][bj][m][0] * s0, v1 = acc[ai][bj][m][1] * s1;
;             u32x4 w; w.x = cvt_pk_bf16(v0[0], v0[1]); w.y = cvt_pk_bf16(v0[2], v0[3]); w.z = cvt_pk_bf16(v1[0], v1[1]); w.w = cvt_pk_bf16(v1[2], v1[3]);
;             *(u32x4*)(merged + (size_t)r * cfg::DM + c) = w; }
.LBB0_1608:
	v_add_u32_e32 v4, s24, v142
	v_ashrrev_i32_e32 v5, 31, v4
	v_or_b32_e32 v180, s26, v218
	v_ashrrev_i32_e32 v181, 31, v180
	s_lshl_b32 s2, s24, 12
	s_lshl_b32 s12, s26, 8
	s_add_i32 s2, s2, s12
	s_lshl_b32 s12, s39, 3
	s_add_i32 s2, s2, s12
	s_add_u32 s12, s6, 0x6001000
	s_addc_u32 s13, s7, 0
	s_add_u32 s12, s12, s2
	s_addc_u32 s13, s13, 0
	v_mbcnt_lo_u32_b32 v150, -1, 0
	v_mbcnt_hi_u32_b32 v150, -1, v150
	v_lshlrev_b32_e32 v150, 3, v150
	v_mov_b32_e32 v151, 0
	v_lshl_add_u64 v[150:151], s[12:13], 0, v[150:151]
	s_mov_b32 s22, 0x3b808081
	s_mov_b32 s2, 0x100000
	s_mov_b64 s[12:13], 0x100000
	global_load_dwordx2 v[182:183], v[150:151], off offset:-4096
	global_load_dwordx2 v[178:179], v[150:151], off offset:-3584
	global_load_dwordx2 v[176:177], v[150:151], off offset:-3072
	global_load_dwordx2 v[174:175], v[150:151], off offset:-2560
	global_load_dwordx2 v[172:173], v[150:151], off offset:-2048
	global_load_dwordx2 v[170:171], v[150:151], off offset:-1536
	global_load_dwordx2 v[168:169], v[150:151], off offset:-1024
	global_load_dwordx2 v[166:167], v[150:151], off offset:-512
	global_load_dwordx2 v[164:165], v[150:151], off
	global_load_dwordx2 v[162:163], v[150:151], off offset:512
	global_load_dwordx2 v[160:161], v[150:151], off offset:1024
	global_load_dwordx2 v[158:159], v[150:151], off offset:1536
	global_load_dwordx2 v[156:157], v[150:151], off offset:2048
	global_load_dwordx2 v[154:155], v[150:151], off offset:2560
	global_load_dwordx2 v[152:153], v[150:151], off offset:3072
	global_load_dwordx2 v[150:151], v[150:151], off offset:3584
	s_waitcnt vmcnt(8)
	v_cvt_f32_ubyte1_e32 v187, v182
	v_cvt_f32_ubyte0_e32 v186, v182
	v_cvt_f32_ubyte3_e32 v185, v182
	v_cvt_f32_ubyte2_e32 v184, v182
	v_pk_mul_f32 v[186:187], v[186:187], s[22:23] op_sel_hi:[1,0]
	v_cvt_f32_ubyte3_e32 v189, v183
	v_cvt_f32_ubyte2_e32 v188, v183
	v_cvt_f32_ubyte1_e32 v191, v183
	v_cvt_f32_ubyte0_e32 v190, v183
	v_pk_mul_f32 v[184:185], v[184:185], s[22:23] op_sel_hi:[1,0]
	v_pk_mul_f32 v[182:183], v[190:191], s[22:23] op_sel_hi:[1,0]
	v_pk_mul_f32 v[188:189], v[188:189], s[22:23] op_sel_hi:[1,0]
	v_pk_mul_f32 v[130:131], v[130:131], v[186:187]
	v_pk_mul_f32 v[132:133], v[132:133], v[184:185]
	v_pk_mul_f32 v[184:185], v[128:129], v[188:189]
	v_pk_mul_f32 v[128:129], v[126:127], v[182:183]
	v_cvt_pk_bf16_f32 v126, v130, v131
	v_lshlrev_b64 v[130:131], 13, v[4:5]
	v_cvt_pk_bf16_f32 v127, v132, v133
	v_lshl_add_u64 v[132:133], s[8:9], 0, v[130:131]
	v_lshlrev_b64 v[130:131], 1, v[180:181]
	v_cvt_pk_bf16_f32 v128, v128, v129
	v_cvt_pk_bf16_f32 v129, v184, v185
	v_lshl_add_u64 v[132:133], v[132:133], 0, v[130:131]
	global_store_dwordx4 v[132:133], v[126:129], off
	v_cvt_f32_ubyte3_e32 v181, v179
	v_cvt_f32_ubyte2_e32 v180, v179
	v_cvt_f32_ubyte3_e32 v127, v178
	v_cvt_f32_ubyte2_e32 v126, v178
	v_cvt_f32_ubyte1_e32 v129, v178
	v_cvt_f32_ubyte0_e32 v128, v178
	v_cvt_f32_ubyte1_e32 v183, v179
	v_cvt_f32_ubyte0_e32 v182, v179
	v_pk_mul_f32 v[128:129], v[128:129], s[22:23] op_sel_hi:[1,0]
	v_pk_mul_f32 v[126:127], v[126:127], s[22:23] op_sel_hi:[1,0]
	v_pk_mul_f32 v[178:179], v[182:183], s[22:23] op_sel_hi:[1,0]
	v_pk_mul_f32 v[180:181], v[180:181], s[22:23] op_sel_hi:[1,0]
	v_pk_mul_f32 v[124:125], v[124:125], v[126:127]
	v_pk_mul_f32 v[122:123], v[122:123], v[128:129]
	v_pk_mul_f32 v[126:127], v[120:121], v[180:181]
	v_pk_mul_f32 v[120:121], v[118:119], v[178:179]
	v_cvt_pk_bf16_f32 v118, v122, v123
	v_cvt_pk_bf16_f32 v119, v124, v125
	v_cvt_pk_bf16_f32 v120, v120, v121
	v_cvt_pk_bf16_f32 v121, v126, v127
	global_store_dwordx4 v[132:133], v[118:121], off offset:256
	v_cvt_f32_ubyte3_e32 v123, v177
	v_cvt_f32_ubyte2_e32 v122, v177
	v_cvt_f32_ubyte1_e32 v121, v176
	v_cvt_f32_ubyte0_e32 v120, v176
	v_cvt_f32_ubyte3_e32 v119, v176
	v_cvt_f32_ubyte2_e32 v118, v176
	v_pk_mul_f32 v[120:121], v[120:121], s[22:23] op_sel_hi:[1,0]
	v_cvt_f32_ubyte1_e32 v125, v177
	v_cvt_f32_ubyte0_e32 v124, v177
	v_or_b32_e32 v126, 16, v4
	v_pk_mul_f32 v[118:119], v[118:119], s[22:23] op_sel_hi:[1,0]
	v_pk_mul_f32 v[124:125], v[124:125], s[22:23] op_sel_hi:[1,0]
	v_pk_mul_f32 v[122:123], v[122:123], s[22:23] op_sel_hi:[1,0]
	v_pk_mul_f32 v[114:115], v[114:115], v[120:121]
	v_ashrrev_i32_e32 v127, 31, v126
	v_pk_mul_f32 v[116:117], v[116:117], v[118:119]
	v_pk_mul_f32 v[118:119], v[112:113], v[122:123]
	v_pk_mul_f32 v[112:113], v[110:111], v[124:125]
	v_cvt_pk_bf16_f32 v110, v114, v115
	v_lshlrev_b64 v[114:115], 13, v[126:127]
	v_lshl_add_u64 v[114:115], s[8:9], 0, v[114:115]
	v_cvt_pk_bf16_f32 v111, v116, v117
	v_cvt_pk_bf16_f32 v112, v112, v113
	v_cvt_pk_bf16_f32 v113, v118, v119
	v_lshl_add_u64 v[114:115], v[114:115], 0, v[130:131]
	global_store_dwordx4 v[114:115], v[110:113], off
	v_cvt_f32_ubyte3_e32 v117, v175
	v_cvt_f32_ubyte2_e32 v116, v175
	v_cvt_f32_ubyte3_e32 v111, v174
	v_cvt_f32_ubyte2_e32 v110, v174
	v_cvt_f32_ubyte1_e32 v113, v174
	v_cvt_f32_ubyte0_e32 v112, v174
	v_cvt_f32_ubyte1_e32 v119, v175
	v_cvt_f32_ubyte0_e32 v118, v175
	v_pk_mul_f32 v[112:113], v[112:113], s[22:23] op_sel_hi:[1,0]
	v_pk_mul_f32 v[110:111], v[110:111], s[22:23] op_sel_hi:[1,0]
	v_pk_mul_f32 v[118:119], v[118:119], s[22:23] op_sel_hi:[1,0]
	v_pk_mul_f32 v[116:117], v[116:117], s[22:23] op_sel_hi:[1,0]
	v_pk_mul_f32 v[108:109], v[108:109], v[110:111]
	v_pk_mul_f32 v[106:107], v[106:107], v[112:113]
	v_pk_mul_f32 v[110:111], v[104:105], v[116:117]
	v_pk_mul_f32 v[104:105], v[102:103], v[118:119]
	v_cvt_pk_bf16_f32 v102, v106, v107
	v_cvt_pk_bf16_f32 v103, v108, v109
	v_cvt_pk_bf16_f32 v104, v104, v105
	v_cvt_pk_bf16_f32 v105, v110, v111
	global_store_dwordx4 v[114:115], v[102:105], off offset:256
; __device__ __forceinline__ unsigned cvt_pk_bf16(float lo, float hi) { f32x2_t v = {lo, hi}; bf16x2_t b = __builtin_convertvector(v, bf16x2_t); return __builtin_bit_cast(unsigned, b); }
;     static __device__ __forceinline__ float ub(unsigned w, int k) { return (float)((w >> (8 * k)) & 0xffu); }
;     __device__ __forceinline__ void operator()(const f32x4 (&acc)[2][2][4][2], const Unit& u, int wr, int wc, int fr, int fq) const {
;     ...
;         for (int i = 0; i < 16; ++i) { const int ai = (i >> 3) & 1, m = (i >> 1) & 3, bj = i & 1; const int r = row0 + ai * HALF + m * 16, c = col0 + bj * HALF;
;             f32x4 s0, s1;
; #pragma unroll
;             for (int j = 0; j < 4; ++j) { s0[j] = ub(ga[i].x, j) * (1.0f / 255.0f); s1[j] = ub(ga[i].y, j) * (1.0f / 255.0f); }
;             const f32x4 v0 = acc[ai][bj][m][0] * s0, v1 = acc[ai][bj][m][1] * s1;
;             u32x4 w; w.x = cvt_pk_bf16(v0[0], v0[1]); w.y = cvt_pk_bf16(v0[2], v0[3]); w.z = cvt_pk_bf16(v1[0], v1[1]); w.w = cvt_pk_bf16(v1[2], v1[3]);
;             *(u32x4*)(merged + (size_t)r * cfg::DM + c) = w; }
	v_cvt_f32_ubyte3_e32 v107, v173
	v_cvt_f32_ubyte2_e32 v106, v173
	v_cvt_f32_ubyte1_e32 v105, v172
	v_cvt_f32_ubyte0_e32 v104, v172
	v_cvt_f32_ubyte3_e32 v103, v172
	v_cvt_f32_ubyte2_e32 v102, v172
	v_pk_mul_f32 v[104:105], v[104:105], s[22:23] op_sel_hi:[1,0]
	v_cvt_f32_ubyte1_e32 v109, v173
	v_cvt_f32_ubyte0_e32 v108, v173
	v_or_b32_e32 v110, 32, v4
	v_pk_mul_f32 v[102:103], v[102:103], s[22:23] op_sel_hi:[1,0]
	v_pk_mul_f32 v[108:109], v[108:109], s[22:23] op_sel_hi:[1,0]
	v_pk_mul_f32 v[106:107], v[106:107], s[22:23] op_sel_hi:[1,0]
	v_pk_mul_f32 v[98:99], v[98:99], v[104:105]
	v_ashrrev_i32_e32 v111, 31, v110
	v_pk_mul_f32 v[100:101], v[100:101], v[102:103]
	v_pk_mul_f32 v[102:103], v[96:97], v[106:107]
	v_pk_mul_f32 v[96:97], v[94:95], v[108:109]
	v_cvt_pk_bf16_f32 v94, v98, v99
	v_lshlrev_b64 v[98:99], 13, v[110:111]
	v_lshl_add_u64 v[98:99], s[8:9], 0, v[98:99]
	v_cvt_pk_bf16_f32 v95, v100, v101
	v_cvt_pk_bf16_f32 v96, v96, v97
	v_cvt_pk_bf16_f32 v97, v102, v103
	v_lshl_add_u64 v[98:99], v[98:99], 0, v[130:131]
	global_store_dwordx4 v[98:99], v[94:97], off
	v_cvt_f32_ubyte3_e32 v101, v171
	v_cvt_f32_ubyte2_e32 v100, v171
	v_cvt_f32_ubyte3_e32 v95, v170
	v_cvt_f32_ubyte2_e32 v94, v170
	v_cvt_f32_ubyte1_e32 v97, v170
	v_cvt_f32_ubyte0_e32 v96, v170
	v_cvt_f32_ubyte1_e32 v103, v171
	v_cvt_f32_ubyte0_e32 v102, v171
	v_pk_mul_f32 v[96:97], v[96:97], s[22:23] op_sel_hi:[1,0]
	v_pk_mul_f32 v[94:95], v[94:95], s[22:23] op_sel_hi:[1,0]
	v_pk_mul_f32 v[102:103], v[102:103], s[22:23] op_sel_hi:[1,0]
	v_pk_mul_f32 v[100:101], v[100:101], s[22:23] op_sel_hi:[1,0]
	v_pk_mul_f32 v[92:93], v[92:93], v[94:95]
	v_pk_mul_f32 v[90:91], v[90:91], v[96:97]
	v_pk_mul_f32 v[94:95], v[88:89], v[100:101]
	v_pk_mul_f32 v[88:89], v[86:87], v[102:103]
	v_cvt_pk_bf16_f32 v86, v90, v91
	v_cvt_pk_bf16_f32 v87, v92, v93
	v_cvt_pk_bf16_f32 v88, v88, v89
	v_cvt_pk_bf16_f32 v89, v94, v95
	global_store_dwordx4 v[98:99], v[86:89], off offset:256
	v_cvt_f32_ubyte3_e32 v91, v169
	v_cvt_f32_ubyte2_e32 v90, v169
	v_cvt_f32_ubyte1_e32 v89, v168
	v_cvt_f32_ubyte0_e32 v88, v168
	v_cvt_f32_ubyte3_e32 v87, v168
	v_cvt_f32_ubyte2_e32 v86, v168
	v_pk_mul_f32 v[88:89], v[88:89], s[22:23] op_sel_hi:[1,0]
	v_cvt_f32_ubyte1_e32 v93, v169
	v_cvt_f32_ubyte0_e32 v92, v169
	v_or_b32_e32 v94, 48, v4
	v_pk_mul_f32 v[86:87], v[86:87], s[22:23] op_sel_hi:[1,0]
	v_pk_mul_f32 v[92:93], v[92:93], s[22:23] op_sel_hi:[1,0]
	v_pk_mul_f32 v[90:91], v[90:91], s[22:23] op_sel_hi:[1,0]
	v_pk_mul_f32 v[82:83], v[82:83], v[88:89]
	v_ashrrev_i32_e32 v95, 31, v94
	v_pk_mul_f32 v[84:85], v[84:85], v[86:87]
	v_pk_mul_f32 v[86:87], v[80:81], v[90:91]
	v_pk_mul_f32 v[80:81], v[78:79], v[92:93]
	v_cvt_pk_bf16_f32 v78, v82, v83
	v_lshlrev_b64 v[82:83], 13, v[94:95]
	v_lshl_add_u64 v[82:83], s[8:9], 0, v[82:83]
	v_cvt_pk_bf16_f32 v79, v84, v85
	v_cvt_pk_bf16_f32 v80, v80, v81
	v_cvt_pk_bf16_f32 v81, v86, v87
	v_lshl_add_u64 v[82:83], v[82:83], 0, v[130:131]
	global_store_dwordx4 v[82:83], v[78:81], off
	v_cvt_f32_ubyte3_e32 v85, v167
	v_cvt_f32_ubyte2_e32 v84, v167
	v_cvt_f32_ubyte3_e32 v79, v166
	v_cvt_f32_ubyte2_e32 v78, v166
	v_cvt_f32_ubyte1_e32 v81, v166
	v_cvt_f32_ubyte0_e32 v80, v166
	v_cvt_f32_ubyte1_e32 v87, v167
	v_cvt_f32_ubyte0_e32 v86, v167
	v_pk_mul_f32 v[80:81], v[80:81], s[22:23] op_sel_hi:[1,0]
	v_pk_mul_f32 v[78:79], v[78:79], s[22:23] op_sel_hi:[1,0]
	v_pk_mul_f32 v[86:87], v[86:87], s[22:23] op_sel_hi:[1,0]
	v_pk_mul_f32 v[84:85], v[84:85], s[22:23] op_sel_hi:[1,0]
	v_pk_mul_f32 v[76:77], v[76:77], v[78:79]
	v_pk_mul_f32 v[74:75], v[74:75], v[80:81]
	v_pk_mul_f32 v[78:79], v[72:73], v[84:85]
	v_pk_mul_f32 v[72:73], v[70:71], v[86:87]
	v_cvt_pk_bf16_f32 v70, v74, v75
	v_cvt_pk_bf16_f32 v71, v76, v77
	v_cvt_pk_bf16_f32 v72, v72, v73
	v_cvt_pk_bf16_f32 v73, v78, v79
	global_store_dwordx4 v[82:83], v[70:73], off offset:256
	s_waitcnt vmcnt(15)
	v_cvt_f32_ubyte3_e32 v75, v165
	v_cvt_f32_ubyte2_e32 v74, v165
	v_cvt_f32_ubyte3_e32 v71, v164
	v_cvt_f32_ubyte2_e32 v70, v164
	v_cvt_f32_ubyte1_e32 v73, v164
	v_cvt_f32_ubyte0_e32 v72, v164
	v_pk_mul_f32 v[70:71], v[70:71], s[22:23] op_sel_hi:[1,0]
	v_cvt_f32_ubyte1_e32 v77, v165
	v_cvt_f32_ubyte0_e32 v76, v165
	v_pk_mul_f32 v[72:73], v[72:73], s[22:23] op_sel_hi:[1,0]
	v_pk_mul_f32 v[76:77], v[76:77], s[22:23] op_sel_hi:[1,0]
	v_pk_mul_f32 v[74:75], v[74:75], s[22:23] op_sel_hi:[1,0]
	v_pk_mul_f32 v[68:69], v[68:69], v[70:71]
	v_pk_mul_f32 v[66:67], v[66:67], v[72:73]
	v_pk_mul_f32 v[70:71], v[64:65], v[74:75]
	v_pk_mul_f32 v[64:65], v[62:63], v[76:77]
	v_cvt_pk_bf16_f32 v63, v68, v69
	v_add_co_u32_e32 v68, vcc, s2, v132
	v_cvt_pk_bf16_f32 v62, v66, v67
	v_cvt_pk_bf16_f32 v64, v64, v65
	v_cvt_pk_bf16_f32 v65, v70, v71
	v_addc_co_u32_e32 v69, vcc, 0, v133, vcc
	global_store_dwordx4 v[68:69], v[62:65], off
	s_waitcnt vmcnt(15)
	v_cvt_f32_ubyte3_e32 v69, v163
	v_cvt_f32_ubyte2_e32 v68, v163
	v_cvt_f32_ubyte3_e32 v63, v162
	v_cvt_f32_ubyte2_e32 v62, v162
	v_cvt_f32_ubyte1_e32 v65, v162
	v_cvt_f32_ubyte0_e32 v64, v162
	v_cvt_f32_ubyte1_e32 v71, v163
	v_cvt_f32_ubyte0_e32 v70, v163
	v_pk_mul_f32 v[64:65], v[64:65], s[22:23] op_sel_hi:[1,0]
	v_pk_mul_f32 v[62:63], v[62:63], s[22:23] op_sel_hi:[1,0]
	v_pk_mul_f32 v[70:71], v[70:71], s[22:23] op_sel_hi:[1,0]
	v_pk_mul_f32 v[68:69], v[68:69], s[22:23] op_sel_hi:[1,0]
	v_pk_mul_f32 v[60:61], v[60:61], v[62:63]
	v_pk_mul_f32 v[58:59], v[58:59], v[64:65]
	v_pk_mul_f32 v[62:63], v[56:57], v[68:69]
	v_pk_mul_f32 v[56:57], v[54:55], v[70:71]
	v_lshl_add_u64 v[66:67], v[132:133], 0, s[12:13]
	v_cvt_pk_bf16_f32 v54, v58, v59
	v_cvt_pk_bf16_f32 v55, v60, v61
	v_cvt_pk_bf16_f32 v56, v56, v57
	v_cvt_pk_bf16_f32 v57, v62, v63
	global_store_dwordx4 v[66:67], v[54:57], off offset:256
	s_waitcnt vmcnt(15)
; __device__ __forceinline__ unsigned cvt_pk_bf16(float lo, float hi) { f32x2_t v = {lo, hi}; bf16x2_t b = __builtin_convertvector(v, bf16x2_t); return __builtin_bit_cast(unsigned, b); }
;     static __device__ __forceinline__ float ub(unsigned w, int k) { return (float)((w >> (8 * k)) & 0xffu); }
; #define PG8_BAR __builtin_amdgcn_s_barrier()
;     __device__ __forceinline__ void operator()(const f32x4 (&acc)[2][2][4][2], const Unit& u, int wr, int wc, int fr, int fq) const {
;     ...
;         for (int i = 0; i < 16; ++i) { const int ai = (i >> 3) & 1, m = (i >> 1) & 3, bj = i & 1; const int r = row0 + ai * HALF + m * 16, c = col0 + bj * HALF;
;             f32x4 s0, s1;
; #pragma unroll
;             for (int j = 0; j < 4; ++j) { s0[j] = ub(ga[i].x, j) * (1.0f / 255.0f); s1[j] = ub(ga[i].y, j) * (1.0f / 255.0f); }
;             const f32x4 v0 = acc[ai][bj][m][0] * s0, v1 = acc[ai][bj][m][1] * s1;
;             u32x4 w; w.x = cvt_pk_bf16(v0[0], v0[1]); w.y = cvt_pk_bf16(v0[2], v0[3]); w.z = cvt_pk_bf16(v1[0], v1[1]); w.w = cvt_pk_bf16(v1[2], v1[3]);
;             *(u32x4*)(merged + (size_t)r * cfg::DM + c) = w; }
; template <class Epi, class Sched, bool ALIGN_EPI = false, bool SP2 = false>
; __device__ __forceinline__ void gemm_phase(PG8_LAS unsigned char* lds, const Gemm g, const Sched& S, const Epi& E) {
;     ...
;         if (!has_next) break;
; #pragma unroll
;         for (int a = 0; a < 2; ++a)
; #pragma unroll
;             for (int b = 0; b < 2; ++b)
; #pragma unroll
;                 for (int m = 0; m < 4; ++m)
; #pragma unroll
;                     for (int n = 0; n < 2; ++n) acc[a][b][m][n] = (f32x4){0.f, 0.f, 0.f, 0.f};
;         cur = nxt; cA = nA; cB = nB; ++ui;
;         if constexpr (ALIGN_EPI) { if (wr == 1) PG8_BAR; }
	v_cvt_f32_ubyte3_e32 v59, v161
	v_cvt_f32_ubyte2_e32 v58, v161
	v_cvt_f32_ubyte1_e32 v57, v160
	v_cvt_f32_ubyte0_e32 v56, v160
	v_cvt_f32_ubyte3_e32 v55, v160
	v_cvt_f32_ubyte2_e32 v54, v160
	v_pk_mul_f32 v[56:57], v[56:57], s[22:23] op_sel_hi:[1,0]
	v_cvt_f32_ubyte1_e32 v61, v161
	v_cvt_f32_ubyte0_e32 v60, v161
	v_add_u32_e32 v62, 0x90, v4
	v_pk_mul_f32 v[54:55], v[54:55], s[22:23] op_sel_hi:[1,0]
	v_pk_mul_f32 v[60:61], v[60:61], s[22:23] op_sel_hi:[1,0]
	v_pk_mul_f32 v[58:59], v[58:59], s[22:23] op_sel_hi:[1,0]
	v_pk_mul_f32 v[50:51], v[50:51], v[56:57]
	v_ashrrev_i32_e32 v63, 31, v62
	v_pk_mul_f32 v[52:53], v[52:53], v[54:55]
	v_pk_mul_f32 v[54:55], v[48:49], v[58:59]
	v_pk_mul_f32 v[48:49], v[46:47], v[60:61]
	v_cvt_pk_bf16_f32 v46, v50, v51
	v_lshlrev_b64 v[50:51], 13, v[62:63]
	v_lshl_add_u64 v[50:51], s[8:9], 0, v[50:51]
	v_cvt_pk_bf16_f32 v47, v52, v53
	v_cvt_pk_bf16_f32 v48, v48, v49
	v_cvt_pk_bf16_f32 v49, v54, v55
	v_lshl_add_u64 v[50:51], v[50:51], 0, v[130:131]
	global_store_dwordx4 v[50:51], v[46:49], off
	s_waitcnt vmcnt(15)
	v_cvt_f32_ubyte3_e32 v53, v159
	v_cvt_f32_ubyte2_e32 v52, v159
	v_cvt_f32_ubyte3_e32 v47, v158
	v_cvt_f32_ubyte2_e32 v46, v158
	v_cvt_f32_ubyte1_e32 v49, v158
	v_cvt_f32_ubyte0_e32 v48, v158
	v_cvt_f32_ubyte1_e32 v55, v159
	v_cvt_f32_ubyte0_e32 v54, v159
	v_pk_mul_f32 v[48:49], v[48:49], s[22:23] op_sel_hi:[1,0]
	v_pk_mul_f32 v[46:47], v[46:47], s[22:23] op_sel_hi:[1,0]
	v_pk_mul_f32 v[54:55], v[54:55], s[22:23] op_sel_hi:[1,0]
	v_pk_mul_f32 v[52:53], v[52:53], s[22:23] op_sel_hi:[1,0]
	v_pk_mul_f32 v[44:45], v[44:45], v[46:47]
	v_pk_mul_f32 v[42:43], v[42:43], v[48:49]
	v_pk_mul_f32 v[46:47], v[40:41], v[52:53]
	v_pk_mul_f32 v[40:41], v[38:39], v[54:55]
	v_cvt_pk_bf16_f32 v38, v42, v43
	v_cvt_pk_bf16_f32 v39, v44, v45
	v_cvt_pk_bf16_f32 v40, v40, v41
	v_cvt_pk_bf16_f32 v41, v46, v47
	global_store_dwordx4 v[50:51], v[38:41], off offset:256
	s_waitcnt vmcnt(15)
	v_cvt_f32_ubyte3_e32 v43, v157
	v_cvt_f32_ubyte2_e32 v42, v157
	v_cvt_f32_ubyte1_e32 v41, v156
	v_cvt_f32_ubyte0_e32 v40, v156
	v_cvt_f32_ubyte3_e32 v39, v156
	v_cvt_f32_ubyte2_e32 v38, v156
	v_pk_mul_f32 v[40:41], v[40:41], s[22:23] op_sel_hi:[1,0]
	v_cvt_f32_ubyte1_e32 v45, v157
	v_cvt_f32_ubyte0_e32 v44, v157
	v_add_u32_e32 v46, 0xa0, v4
	v_pk_mul_f32 v[38:39], v[38:39], s[22:23] op_sel_hi:[1,0]
	v_pk_mul_f32 v[44:45], v[44:45], s[22:23] op_sel_hi:[1,0]
	v_pk_mul_f32 v[42:43], v[42:43], s[22:23] op_sel_hi:[1,0]
	v_pk_mul_f32 v[34:35], v[34:35], v[40:41]
	v_ashrrev_i32_e32 v47, 31, v46
	v_pk_mul_f32 v[36:37], v[36:37], v[38:39]
	v_pk_mul_f32 v[38:39], v[32:33], v[42:43]
	v_pk_mul_f32 v[32:33], v[30:31], v[44:45]
	v_cvt_pk_bf16_f32 v30, v34, v35
	v_lshlrev_b64 v[34:35], 13, v[46:47]
	v_lshl_add_u64 v[34:35], s[8:9], 0, v[34:35]
	v_cvt_pk_bf16_f32 v31, v36, v37
	v_cvt_pk_bf16_f32 v32, v32, v33
	v_cvt_pk_bf16_f32 v33, v38, v39
	v_lshl_add_u64 v[34:35], v[34:35], 0, v[130:131]
	global_store_dwordx4 v[34:35], v[30:33], off
	s_waitcnt vmcnt(15)
	v_cvt_f32_ubyte3_e32 v37, v155
	v_cvt_f32_ubyte2_e32 v36, v155
	v_cvt_f32_ubyte3_e32 v31, v154
	v_cvt_f32_ubyte2_e32 v30, v154
	v_cvt_f32_ubyte1_e32 v33, v154
	v_cvt_f32_ubyte0_e32 v32, v154
	v_cvt_f32_ubyte1_e32 v39, v155
	v_cvt_f32_ubyte0_e32 v38, v155
	v_pk_mul_f32 v[32:33], v[32:33], s[22:23] op_sel_hi:[1,0]
	v_pk_mul_f32 v[30:31], v[30:31], s[22:23] op_sel_hi:[1,0]
	v_pk_mul_f32 v[38:39], v[38:39], s[22:23] op_sel_hi:[1,0]
	v_pk_mul_f32 v[36:37], v[36:37], s[22:23] op_sel_hi:[1,0]
	v_pk_mul_f32 v[28:29], v[28:29], v[30:31]
	v_pk_mul_f32 v[26:27], v[26:27], v[32:33]
	v_pk_mul_f32 v[30:31], v[24:25], v[36:37]
	v_pk_mul_f32 v[24:25], v[22:23], v[38:39]
	v_cvt_pk_bf16_f32 v22, v26, v27
	v_cvt_pk_bf16_f32 v23, v28, v29
	v_cvt_pk_bf16_f32 v24, v24, v25
	v_cvt_pk_bf16_f32 v25, v30, v31
	v_add_u32_e32 v4, 0xb0, v4
	global_store_dwordx4 v[34:35], v[22:25], off offset:256
	s_waitcnt vmcnt(15)
	v_cvt_f32_ubyte3_e32 v27, v153
	v_cvt_f32_ubyte2_e32 v26, v153
	v_cvt_f32_ubyte3_e32 v23, v152
	v_cvt_f32_ubyte2_e32 v22, v152
	v_cvt_f32_ubyte1_e32 v25, v152
	v_cvt_f32_ubyte0_e32 v24, v152
	v_cvt_f32_ubyte1_e32 v29, v153
	v_cvt_f32_ubyte0_e32 v28, v153
	v_ashrrev_i32_e32 v5, 31, v4
	v_pk_mul_f32 v[24:25], v[24:25], s[22:23] op_sel_hi:[1,0]
	v_pk_mul_f32 v[22:23], v[22:23], s[22:23] op_sel_hi:[1,0]
	v_pk_mul_f32 v[28:29], v[28:29], s[22:23] op_sel_hi:[1,0]
	v_pk_mul_f32 v[26:27], v[26:27], s[22:23] op_sel_hi:[1,0]
	v_lshlrev_b64 v[4:5], 13, v[4:5]
	v_pk_mul_f32 v[20:21], v[20:21], v[22:23]
	v_pk_mul_f32 v[18:19], v[18:19], v[24:25]
	v_pk_mul_f32 v[22:23], v[16:17], v[26:27]
	v_pk_mul_f32 v[16:17], v[14:15], v[28:29]
	v_lshl_add_u64 v[4:5], s[8:9], 0, v[4:5]
	v_cvt_pk_bf16_f32 v14, v18, v19
	v_cvt_pk_bf16_f32 v15, v20, v21
	v_cvt_pk_bf16_f32 v16, v16, v17
	v_cvt_pk_bf16_f32 v17, v22, v23
	v_lshl_add_u64 v[18:19], v[4:5], 0, v[130:131]
	global_store_dwordx4 v[18:19], v[14:17], off
	s_waitcnt vmcnt(15)
	v_cvt_f32_ubyte3_e32 v5, v150
	v_cvt_f32_ubyte2_e32 v4, v150
	v_cvt_f32_ubyte1_e32 v15, v150
	v_cvt_f32_ubyte0_e32 v14, v150
	v_cvt_f32_ubyte3_e32 v17, v151
	v_cvt_f32_ubyte2_e32 v16, v151
	v_cvt_f32_ubyte1_e32 v21, v151
	v_cvt_f32_ubyte0_e32 v20, v151
	v_pk_mul_f32 v[14:15], v[14:15], s[22:23] op_sel_hi:[1,0]
	v_pk_mul_f32 v[4:5], v[4:5], s[22:23] op_sel_hi:[1,0]
	v_pk_mul_f32 v[20:21], v[20:21], s[22:23] op_sel_hi:[1,0]
	v_pk_mul_f32 v[16:17], v[16:17], s[22:23] op_sel_hi:[1,0]
	v_pk_mul_f32 v[12:13], v[12:13], v[4:5]
	v_pk_mul_f32 v[4:5], v[10:11], v[14:15]
	v_pk_mul_f32 v[8:9], v[8:9], v[16:17]
	v_pk_mul_f32 v[6:7], v[6:7], v[20:21]
	v_cvt_pk_bf16_f32 v4, v4, v5
	v_cvt_pk_bf16_f32 v5, v12, v13
	v_cvt_pk_bf16_f32 v6, v6, v7
	v_cvt_pk_bf16_f32 v7, v8, v9
	s_mov_b64 s[12:13], -1
	s_andn2_b64 vcc, exec, s[0:1]
	global_store_dwordx4 v[18:19], v[4:7], off offset:256
	s_cbranch_vccnz .LBB0_1594
	s_andn2_b64 vcc, exec, s[4:5]
	s_cbranch_vccnz .LBB0_1593
	s_barrier
	s_branch .LBB0_1593

; __global__ void __launch_bounds__(NWAVES * 64, 2) mega_fwd(Args args) {
	.amdhsa_kernel _Z8mega_fwd4Args
		.amdhsa_group_segment_fixed_size 0
		.amdhsa_private_segment_fixed_size 0
		.amdhsa_kernarg_size 432
		.amdhsa_user_sgpr_count 2
		.amdhsa_user_sgpr_dispatch_ptr 0
		.amdhsa_user_sgpr_queue_ptr 0
		.amdhsa_user_sgpr_kernarg_segment_ptr 1
		.amdhsa_user_sgpr_dispatch_id 0
		.amdhsa_user_sgpr_kernarg_preload_length 0
		.amdhsa_user_sgpr_kernarg_preload_offset 0
		.amdhsa_user_sgpr_private_segment_size 0
		.amdhsa_uses_dynamic_stack 0
		.amdhsa_enable_private_segment 0
		.amdhsa_system_sgpr_workgroup_id_x 1
		.amdhsa_system_sgpr_workgroup_id_y 0
		.amdhsa_system_sgpr_workgroup_id_z 0
		.amdhsa_system_sgpr_workgroup_info 0
		.amdhsa_system_vgpr_workitem_id 0
		.amdhsa_next_free_vgpr 256
		.amdhsa_next_free_sgpr 102
		.amdhsa_accum_offset 256
		.amdhsa_reserve_vcc 1
		.amdhsa_float_round_mode_32 0
		.amdhsa_float_round_mode_16_64 0
		.amdhsa_float_denorm_mode_32 3
		.amdhsa_float_denorm_mode_16_64 3
		.amdhsa_dx10_clamp 1
		.amdhsa_ieee_mode 1
		.amdhsa_fp16_overflow 0
		.amdhsa_tg_split 0
		.amdhsa_exception_fp_ieee_invalid_op 0
		.amdhsa_exception_fp_denorm_src 0
		.amdhsa_exception_fp_ieee_div_zero 0
		.amdhsa_exception_fp_ieee_overflow 0
		.amdhsa_exception_fp_ieee_underflow 0
		.amdhsa_exception_fp_ieee_inexact 0
		.amdhsa_exception_int_div_zero 0
	.end_amdhsa_kernel

; __global__ void __launch_bounds__(NWAVES * 64, 2) mega_fwd(Args args) {
amdhsa.kernels:
  - .agpr_count:     0
    .args:
      - .offset:         0
        .size:           176
        .value_kind:     by_value
      - .offset:         176
        .size:           4
        .value_kind:     hidden_block_count_x
      - .offset:         180
        .size:           4
        .value_kind:     hidden_block_count_y
      - .offset:         184
        .size:           4
        .value_kind:     hidden_block_count_z
      - .offset:         188
        .size:           2
        .value_kind:     hidden_group_size_x
      - .offset:         190
        .size:           2
        .value_kind:     hidden_group_size_y
      - .offset:         192
        .size:           2
        .value_kind:     hidden_group_size_z
      - .offset:         194
        .size:           2
        .value_kind:     hidden_remainder_x
      - .offset:         196
        .size:           2
        .value_kind:     hidden_remainder_y
      - .offset:         198
        .size:           2
        .value_kind:     hidden_remainder_z
      - .offset:         216
        .size:           8
        .value_kind:     hidden_global_offset_x
      - .offset:         224
        .size:           8
        .value_kind:     hidden_global_offset_y
      - .offset:         232
        .size:           8
        .value_kind:     hidden_global_offset_z
      - .offset:         240
        .size:           2
        .value_kind:     hidden_grid_dims
      - .offset:         296
        .size:           4
        .value_kind:     hidden_dynamic_lds_size
    .group_segment_fixed_size: 0
    .kernarg_segment_align: 8
    .kernarg_segment_size: 432
    .language:       OpenCL C
    .language_version:
      - 2
      - 0
    .max_flat_workgroup_size: 512
    .name:           _Z8mega_fwd4Args
    .private_segment_fixed_size: 0
    .sgpr_count:     108
    .sgpr_spill_count: 227
    .symbol:         _Z8mega_fwd4Args.kd
    .uniform_work_group_size: 1
    .uses_dynamic_stack: false
    .vgpr_count:     256
    .vgpr_spill_count: 0
    .wavefront_size: 64
